# t5 + one combined s_waitcnt vmcnt(8) lgkmcnt(0) before each GEMM mid barrier; s_setprio 0 moved after the end barrier (36 sites each)
# speedup vs baseline: 1.0010x; 1.0010x over previous
.LBB0_234:
	s_add_i32 s63, 0, 0x10000
	s_add_i32 s66, 0, 0x14000
	v_add_u32_e32 v134, s63, v165
	v_add_u32_e32 v160, s66, v165
	ds_read_b128 v[114:117], v134
	ds_read_b128 v[118:121], v134 offset:1024
	ds_read_b128 v[130:133], v134 offset:2048
	ds_read_b128 v[134:137], v134 offset:3072
	ds_read_b128 v[170:173], v160
	ds_read_b128 v[174:177], v160 offset:1024
	ds_read_b128 v[200:203], v160 offset:2048
	ds_read_b128 v[204:207], v160 offset:3072
	ds_read_b128 v[208:211], v168
	ds_read_b128 v[212:215], v168 offset:1024
	ds_read_b128 v[216:219], v168 offset:2048
	ds_read_b128 v[220:223], v168 offset:3072
	ds_read_b128 v[224:227], v168 offset:4096
	ds_read_b128 v[228:231], v168 offset:5120
	ds_read_b128 v[232:235], v168 offset:6144
	ds_read_b128 v[236:239], v168 offset:7168
	s_add_u32 s38, s0, 0xfffc0080
	s_addc_u32 s39, s1, -1
	s_cmp_eq_u32 s62, 12
	s_cselect_b32 s41, s25, s39
	s_cselect_b32 s40, s58, s38
	s_cselect_b32 s39, s27, s61
	s_cselect_b32 s38, s59, s60
	v_lshl_add_u64 v[160:161], s[0:1], 0, v[158:159]
	s_add_i32 m0, s37, 0xc000
	s_nop 0
	global_load_lds_dwordx4 v[160:161], off
	v_lshl_add_u64 v[160:161], s[0:1], 0, v[156:157]
	s_add_i32 m0, s37, 0xe000
	s_nop 0
	global_load_lds_dwordx4 v[160:161], off
	s_waitcnt vmcnt(8) lgkmcnt(0)
	s_setprio 1
	s_barrier
	v_mfma_f32_16x16x32_bf16 v[142:145], v[114:117], v[208:211], v[142:145]
	v_mfma_f32_16x16x32_bf16 v[138:141], v[130:133], v[208:211], v[138:141]
	v_mfma_f32_16x16x32_bf16 v[110:113], v[114:117], v[216:219], v[110:113]
	v_mfma_f32_16x16x32_bf16 v[106:109], v[130:133], v[216:219], v[106:109]
	v_mfma_f32_16x16x32_bf16 v[94:97], v[114:117], v[224:227], v[94:97]
	v_mfma_f32_16x16x32_bf16 v[90:93], v[130:133], v[224:227], v[90:93]
	v_mfma_f32_16x16x32_bf16 v[78:81], v[114:117], v[232:235], v[78:81]
	v_mfma_f32_16x16x32_bf16 v[74:77], v[130:133], v[232:235], v[74:77]
	v_mfma_f32_16x16x32_bf16 v[142:145], v[118:121], v[212:215], v[142:145]
	v_mfma_f32_16x16x32_bf16 v[138:141], v[134:137], v[212:215], v[138:141]
	v_mfma_f32_16x16x32_bf16 v[110:113], v[118:121], v[220:223], v[110:113]
	v_mfma_f32_16x16x32_bf16 v[106:109], v[134:137], v[220:223], v[106:109]
	v_mfma_f32_16x16x32_bf16 v[94:97], v[118:121], v[228:231], v[94:97]
	v_mfma_f32_16x16x32_bf16 v[90:93], v[134:137], v[228:231], v[90:93]
	v_mfma_f32_16x16x32_bf16 v[78:81], v[118:121], v[236:239], v[78:81]
	v_mfma_f32_16x16x32_bf16 v[74:77], v[134:137], v[236:239], v[74:77]
	s_setprio 0
	s_setprio 1
	v_mfma_f32_16x16x32_bf16 v[126:129], v[170:173], v[208:211], v[126:129]
	v_mfma_f32_16x16x32_bf16 v[122:125], v[200:203], v[208:211], v[122:125]
	v_mfma_f32_16x16x32_bf16 v[102:105], v[170:173], v[216:219], v[102:105]
	v_mfma_f32_16x16x32_bf16 v[98:101], v[200:203], v[216:219], v[98:101]
	v_mfma_f32_16x16x32_bf16 v[86:89], v[170:173], v[224:227], v[86:89]
	v_mfma_f32_16x16x32_bf16 v[82:85], v[200:203], v[224:227], v[82:85]
	v_mfma_f32_16x16x32_bf16 v[70:73], v[170:173], v[232:235], v[70:73]
	v_mfma_f32_16x16x32_bf16 v[66:69], v[200:203], v[232:235], v[66:69]
	v_mfma_f32_16x16x32_bf16 v[126:129], v[174:177], v[212:215], v[126:129]
	v_mfma_f32_16x16x32_bf16 v[122:125], v[204:207], v[212:215], v[122:125]
	v_mfma_f32_16x16x32_bf16 v[102:105], v[174:177], v[220:223], v[102:105]
	v_mfma_f32_16x16x32_bf16 v[98:101], v[204:207], v[220:223], v[98:101]
	v_mfma_f32_16x16x32_bf16 v[86:89], v[174:177], v[228:231], v[86:89]
	v_mfma_f32_16x16x32_bf16 v[82:85], v[204:207], v[228:231], v[82:85]
	v_mfma_f32_16x16x32_bf16 v[70:73], v[174:177], v[236:239], v[70:73]
	v_mfma_f32_16x16x32_bf16 v[66:69], v[204:207], v[236:239], v[66:69]
	s_barrier
	s_setprio 0
	ds_read_b128 v[208:211], v168 offset:16384
	ds_read_b128 v[212:215], v168 offset:17408
	ds_read_b128 v[216:219], v168 offset:18432
	ds_read_b128 v[220:223], v168 offset:19456
	ds_read_b128 v[224:227], v168 offset:20480
	ds_read_b128 v[228:231], v168 offset:21504
	ds_read_b128 v[232:235], v168 offset:22528
	ds_read_b128 v[236:239], v168 offset:23552
	s_add_i32 s63, s63, s42
	v_lshl_add_u64 v[160:161], s[38:39], 0, v[146:147]
	s_mov_b32 m0, s63
	s_nop 0
	global_load_lds_dwordx4 v[160:161], off
	s_add_i32 m0, s63, 0x2000
	s_add_u32 s64, s38, 0x40000
	v_lshl_add_u64 v[178:179], s[38:39], 0, v[148:149]
	s_addc_u32 s65, s39, 0
	s_add_i32 s63, s66, s42
	global_load_lds_dwordx4 v[178:179], off
	v_lshl_add_u64 v[240:241], s[64:65], 0, v[146:147]
	s_mov_b32 m0, s63
	v_lshl_add_u64 v[242:243], s[40:41], 0, v[148:149]
	global_load_lds_dwordx4 v[240:241], off
	v_lshl_add_u64 v[240:241], s[64:65], 0, v[148:149]
	s_add_i32 m0, s63, 0x2000
	s_nop 0
	global_load_lds_dwordx4 v[240:241], off
	v_lshl_add_u64 v[240:241], s[40:41], 0, v[146:147]
	s_mov_b32 m0, s37
	s_nop 0
	global_load_lds_dwordx4 v[240:241], off
	s_mov_b32 m0, s47
	s_nop 0
	global_load_lds_dwordx4 v[242:243], off
	s_waitcnt vmcnt(8) lgkmcnt(0)
	s_setprio 1
	s_barrier
	v_mfma_f32_16x16x32_bf16 v[62:65], v[114:117], v[208:211], v[62:65]
	v_mfma_f32_16x16x32_bf16 v[58:61], v[130:133], v[208:211], v[58:61]
	v_mfma_f32_16x16x32_bf16 v[46:49], v[114:117], v[216:219], v[46:49]
	v_mfma_f32_16x16x32_bf16 v[42:45], v[130:133], v[216:219], v[42:45]
	v_mfma_f32_16x16x32_bf16 v[30:33], v[114:117], v[224:227], v[30:33]
	v_mfma_f32_16x16x32_bf16 v[26:29], v[130:133], v[224:227], v[26:29]
	v_mfma_f32_16x16x32_bf16 v[14:17], v[114:117], v[232:235], v[14:17]
	v_mfma_f32_16x16x32_bf16 v[10:13], v[130:133], v[232:235], v[10:13]
	v_mfma_f32_16x16x32_bf16 v[62:65], v[118:121], v[212:215], v[62:65]
	v_mfma_f32_16x16x32_bf16 v[58:61], v[134:137], v[212:215], v[58:61]
	v_mfma_f32_16x16x32_bf16 v[46:49], v[118:121], v[220:223], v[46:49]
	v_mfma_f32_16x16x32_bf16 v[42:45], v[134:137], v[220:223], v[42:45]
	v_mfma_f32_16x16x32_bf16 v[30:33], v[118:121], v[228:231], v[30:33]
	v_mfma_f32_16x16x32_bf16 v[26:29], v[134:137], v[228:231], v[26:29]
	v_mfma_f32_16x16x32_bf16 v[14:17], v[118:121], v[236:239], v[14:17]
	v_mfma_f32_16x16x32_bf16 v[10:13], v[134:137], v[236:239], v[10:13]
	s_setprio 0
	s_setprio 1
	v_mfma_f32_16x16x32_bf16 v[54:57], v[170:173], v[208:211], v[54:57]
	v_mfma_f32_16x16x32_bf16 v[50:53], v[200:203], v[208:211], v[50:53]
	v_mfma_f32_16x16x32_bf16 v[38:41], v[170:173], v[216:219], v[38:41]
	v_mfma_f32_16x16x32_bf16 v[34:37], v[200:203], v[216:219], v[34:37]
	v_mfma_f32_16x16x32_bf16 v[22:25], v[170:173], v[224:227], v[22:25]
	v_mfma_f32_16x16x32_bf16 v[18:21], v[200:203], v[224:227], v[18:21]
	v_mfma_f32_16x16x32_bf16 v[6:9], v[170:173], v[232:235], v[6:9]
	v_mfma_f32_16x16x32_bf16 v[2:5], v[200:203], v[232:235], v[2:5]
	v_mfma_f32_16x16x32_bf16 v[54:57], v[174:177], v[212:215], v[54:57]
	v_mfma_f32_16x16x32_bf16 v[50:53], v[204:207], v[212:215], v[50:53]
	v_mfma_f32_16x16x32_bf16 v[38:41], v[174:177], v[220:223], v[38:41]
	v_mfma_f32_16x16x32_bf16 v[34:37], v[204:207], v[220:223], v[34:37]
	v_mfma_f32_16x16x32_bf16 v[22:25], v[174:177], v[228:231], v[22:25]
	v_mfma_f32_16x16x32_bf16 v[18:21], v[204:207], v[228:231], v[18:21]
	v_mfma_f32_16x16x32_bf16 v[6:9], v[174:177], v[236:239], v[6:9]
	v_mfma_f32_16x16x32_bf16 v[2:5], v[204:207], v[236:239], v[2:5]
	s_barrier
	s_setprio 0
	s_add_i32 s63, 0, 0x18000
	s_add_i32 s64, 0, 0x1c000
	v_add_u32_e32 v134, s63, v165
	v_add_u32_e32 v162, s64, v165
	ds_read_b128 v[114:117], v134
	ds_read_b128 v[118:121], v134 offset:1024
	ds_read_b128 v[130:133], v134 offset:2048
	ds_read_b128 v[134:137], v134 offset:3072
	ds_read_b128 v[170:173], v162
	ds_read_b128 v[174:177], v162 offset:1024
	ds_read_b128 v[200:203], v162 offset:2048
	ds_read_b128 v[204:207], v162 offset:3072
	ds_read_b128 v[208:211], v168 offset:32768
	ds_read_b128 v[212:215], v168 offset:33792
	ds_read_b128 v[216:219], v168 offset:34816
	ds_read_b128 v[220:223], v168 offset:35840
	ds_read_b128 v[224:227], v168 offset:36864
	ds_read_b128 v[228:231], v168 offset:37888
	ds_read_b128 v[232:235], v168 offset:38912
	ds_read_b128 v[236:239], v168 offset:39936
	s_add_u32 s40, s40, 0x40000
	s_addc_u32 s41, s41, 0
	s_mov_b32 m0, s48
	v_lshl_add_u64 v[244:245], s[40:41], 0, v[146:147]
	global_load_lds_dwordx4 v[244:245], off
	v_lshl_add_u64 v[244:245], s[40:41], 0, v[148:149]
	s_mov_b32 m0, s49
	s_nop 0
	global_load_lds_dwordx4 v[244:245], off
	s_waitcnt vmcnt(8) lgkmcnt(0)
	s_setprio 1
	s_barrier
	v_mfma_f32_16x16x32_bf16 v[142:145], v[114:117], v[208:211], v[142:145]
	v_mfma_f32_16x16x32_bf16 v[138:141], v[130:133], v[208:211], v[138:141]
	v_mfma_f32_16x16x32_bf16 v[110:113], v[114:117], v[216:219], v[110:113]
	v_mfma_f32_16x16x32_bf16 v[106:109], v[130:133], v[216:219], v[106:109]
	v_mfma_f32_16x16x32_bf16 v[94:97], v[114:117], v[224:227], v[94:97]
	v_mfma_f32_16x16x32_bf16 v[90:93], v[130:133], v[224:227], v[90:93]
	v_mfma_f32_16x16x32_bf16 v[78:81], v[114:117], v[232:235], v[78:81]
	v_mfma_f32_16x16x32_bf16 v[74:77], v[130:133], v[232:235], v[74:77]
	v_mfma_f32_16x16x32_bf16 v[142:145], v[118:121], v[212:215], v[142:145]
	v_mfma_f32_16x16x32_bf16 v[138:141], v[134:137], v[212:215], v[138:141]
	v_mfma_f32_16x16x32_bf16 v[110:113], v[118:121], v[220:223], v[110:113]
	v_mfma_f32_16x16x32_bf16 v[106:109], v[134:137], v[220:223], v[106:109]
	v_mfma_f32_16x16x32_bf16 v[94:97], v[118:121], v[228:231], v[94:97]
	v_mfma_f32_16x16x32_bf16 v[90:93], v[134:137], v[228:231], v[90:93]
	v_mfma_f32_16x16x32_bf16 v[78:81], v[118:121], v[236:239], v[78:81]
	v_mfma_f32_16x16x32_bf16 v[74:77], v[134:137], v[236:239], v[74:77]
	s_setprio 0
	s_setprio 1
	v_mfma_f32_16x16x32_bf16 v[126:129], v[170:173], v[208:211], v[126:129]
	v_mfma_f32_16x16x32_bf16 v[122:125], v[200:203], v[208:211], v[122:125]
	v_mfma_f32_16x16x32_bf16 v[102:105], v[170:173], v[216:219], v[102:105]
	v_mfma_f32_16x16x32_bf16 v[98:101], v[200:203], v[216:219], v[98:101]
	v_mfma_f32_16x16x32_bf16 v[86:89], v[170:173], v[224:227], v[86:89]
	v_mfma_f32_16x16x32_bf16 v[82:85], v[200:203], v[224:227], v[82:85]
	v_mfma_f32_16x16x32_bf16 v[70:73], v[170:173], v[232:235], v[70:73]
	v_mfma_f32_16x16x32_bf16 v[66:69], v[200:203], v[232:235], v[66:69]
	v_mfma_f32_16x16x32_bf16 v[126:129], v[174:177], v[212:215], v[126:129]
	v_mfma_f32_16x16x32_bf16 v[122:125], v[204:207], v[212:215], v[122:125]
	v_mfma_f32_16x16x32_bf16 v[102:105], v[174:177], v[220:223], v[102:105]
	v_mfma_f32_16x16x32_bf16 v[98:101], v[204:207], v[220:223], v[98:101]
	v_mfma_f32_16x16x32_bf16 v[86:89], v[174:177], v[228:231], v[86:89]
	v_mfma_f32_16x16x32_bf16 v[82:85], v[204:207], v[228:231], v[82:85]
	v_mfma_f32_16x16x32_bf16 v[70:73], v[174:177], v[236:239], v[70:73]
	v_mfma_f32_16x16x32_bf16 v[66:69], v[204:207], v[236:239], v[66:69]
	s_barrier
	s_setprio 0
	ds_read_b128 v[208:211], v168 offset:49152
	ds_read_b128 v[212:215], v168 offset:50176
	ds_read_b128 v[216:219], v168 offset:51200
	ds_read_b128 v[220:223], v168 offset:52224
	ds_read_b128 v[224:227], v168 offset:53248
	ds_read_b128 v[228:231], v168 offset:54272
	ds_read_b128 v[232:235], v168 offset:55296
	ds_read_b128 v[236:239], v168 offset:56320
	s_add_i32 s40, s63, s42
	v_lshl_add_u64 v[160:161], v[160:161], 0, s[90:91]
	s_mov_b32 m0, s40
	s_nop 0
	global_load_lds_dwordx4 v[160:161], off
	s_add_i32 m0, s40, 0x2000
	s_add_u32 s38, s38, 0x40080
	v_lshl_add_u64 v[160:161], v[178:179], 0, s[90:91]
	s_addc_u32 s39, s39, 0
	s_add_i32 s40, s64, s42
	global_load_lds_dwordx4 v[160:161], off
	v_lshl_add_u64 v[160:161], s[38:39], 0, v[146:147]
	s_mov_b32 m0, s40
	s_nop 0
	global_load_lds_dwordx4 v[160:161], off
	v_lshl_add_u64 v[160:161], s[38:39], 0, v[148:149]
	s_add_i32 m0, s40, 0x2000
	s_nop 0
	global_load_lds_dwordx4 v[160:161], off
	v_lshl_add_u64 v[160:161], v[240:241], 0, s[90:91]
	s_mov_b32 m0, s52
	s_nop 0
	global_load_lds_dwordx4 v[160:161], off
	v_lshl_add_u64 v[160:161], v[242:243], 0, s[90:91]
	s_mov_b32 m0, s53
	s_nop 0
	global_load_lds_dwordx4 v[160:161], off
	s_waitcnt vmcnt(8) lgkmcnt(0)
	s_setprio 1
	s_barrier
	v_mfma_f32_16x16x32_bf16 v[62:65], v[114:117], v[208:211], v[62:65]
	v_mfma_f32_16x16x32_bf16 v[58:61], v[130:133], v[208:211], v[58:61]
	v_mfma_f32_16x16x32_bf16 v[46:49], v[114:117], v[216:219], v[46:49]
	v_mfma_f32_16x16x32_bf16 v[42:45], v[130:133], v[216:219], v[42:45]
	v_mfma_f32_16x16x32_bf16 v[30:33], v[114:117], v[224:227], v[30:33]
	v_mfma_f32_16x16x32_bf16 v[26:29], v[130:133], v[224:227], v[26:29]
	v_mfma_f32_16x16x32_bf16 v[14:17], v[114:117], v[232:235], v[14:17]
	v_mfma_f32_16x16x32_bf16 v[10:13], v[130:133], v[232:235], v[10:13]
	v_mfma_f32_16x16x32_bf16 v[62:65], v[118:121], v[212:215], v[62:65]
	v_mfma_f32_16x16x32_bf16 v[58:61], v[134:137], v[212:215], v[58:61]
	v_mfma_f32_16x16x32_bf16 v[46:49], v[118:121], v[220:223], v[46:49]
	v_mfma_f32_16x16x32_bf16 v[42:45], v[134:137], v[220:223], v[42:45]
	v_mfma_f32_16x16x32_bf16 v[30:33], v[118:121], v[228:231], v[30:33]
	v_mfma_f32_16x16x32_bf16 v[26:29], v[134:137], v[228:231], v[26:29]
	v_mfma_f32_16x16x32_bf16 v[14:17], v[118:121], v[236:239], v[14:17]
	v_mfma_f32_16x16x32_bf16 v[10:13], v[134:137], v[236:239], v[10:13]
	s_setprio 0
	s_setprio 1
	v_mfma_f32_16x16x32_bf16 v[54:57], v[170:173], v[208:211], v[54:57]
	v_mfma_f32_16x16x32_bf16 v[50:53], v[200:203], v[208:211], v[50:53]
	v_mfma_f32_16x16x32_bf16 v[38:41], v[170:173], v[216:219], v[38:41]
	v_mfma_f32_16x16x32_bf16 v[34:37], v[200:203], v[216:219], v[34:37]
	v_mfma_f32_16x16x32_bf16 v[22:25], v[170:173], v[224:227], v[22:25]
	v_mfma_f32_16x16x32_bf16 v[18:21], v[200:203], v[224:227], v[18:21]
	v_mfma_f32_16x16x32_bf16 v[6:9], v[170:173], v[232:235], v[6:9]
	v_mfma_f32_16x16x32_bf16 v[2:5], v[200:203], v[232:235], v[2:5]
	v_mfma_f32_16x16x32_bf16 v[54:57], v[174:177], v[212:215], v[54:57]
	v_mfma_f32_16x16x32_bf16 v[50:53], v[204:207], v[212:215], v[50:53]
	v_mfma_f32_16x16x32_bf16 v[38:41], v[174:177], v[220:223], v[38:41]
	v_mfma_f32_16x16x32_bf16 v[34:37], v[204:207], v[220:223], v[34:37]
	v_mfma_f32_16x16x32_bf16 v[22:25], v[174:177], v[228:231], v[22:25]
	v_mfma_f32_16x16x32_bf16 v[18:21], v[204:207], v[228:231], v[18:21]
	v_mfma_f32_16x16x32_bf16 v[6:9], v[174:177], v[236:239], v[6:9]
	v_mfma_f32_16x16x32_bf16 v[2:5], v[204:207], v[236:239], v[2:5]
	s_barrier
	s_setprio 0
	s_add_i32 s62, s62, 2
	s_add_u32 s60, s60, 0x100
	s_addc_u32 s61, s61, 0
	s_add_u32 s0, s0, 0x100
	s_addc_u32 s1, s1, 0
	s_cmp_lt_u32 s62, 14
	s_cbranch_scc1 .LBB0_234
	s_andn2_b64 vcc, exec, s[22:23]
	s_cbranch_vccnz .LBB0_237
	s_barrier

.LBB0_318:
	s_add_u32 s41, s10, s40
	s_addc_u32 s42, s11, 0
	s_add_u32 s43, s41, 0x100
	s_addc_u32 s44, s42, 0
	s_and_b64 s[24:25], s[22:23], exec
	s_cselect_b32 s25, s15, s44
	s_cselect_b32 s24, s39, s43
	s_add_u32 s40, s8, s40
	s_addc_u32 s43, s9, 0
	s_add_u32 s40, s40, 0x100
	s_addc_u32 s43, s43, 0
	s_add_i32 s44, 0, 0x10000
	s_and_b64 s[22:23], s[22:23], exec
	v_add_u32_e32 v141, s44, v139
	s_cselect_b32 s23, s17, s43
	s_cselect_b32 s22, s16, s40
	s_add_i32 s43, 0, 0x14000
	ds_read_b128 v[142:145], v141
	ds_read_b128 v[146:149], v141 offset:1024
	ds_read_b128 v[150:153], v141 offset:2048
	ds_read_b128 v[154:157], v141 offset:3072
	v_add_u32_e32 v141, s43, v139
	ds_read_b128 v[158:161], v141
	ds_read_b128 v[164:167], v141 offset:1024
	ds_read_b128 v[168:171], v141 offset:2048
	ds_read_b128 v[172:175], v141 offset:3072
	s_add_u32 s40, s41, 0x20080
	s_addc_u32 s41, s42, 0
	v_lshl_add_u64 v[228:229], s[40:41], 0, v[130:131]
	s_add_i32 m0, s7, 0xc000
	ds_read_b128 v[176:179], v140
	ds_read_b128 v[200:203], v140 offset:1024
	ds_read_b128 v[204:207], v140 offset:2048
	ds_read_b128 v[208:211], v140 offset:3072
	ds_read_b128 v[212:215], v140 offset:4096
	ds_read_b128 v[216:219], v140 offset:5120
	ds_read_b128 v[220:223], v140 offset:6144
	ds_read_b128 v[224:227], v140 offset:7168
	global_load_lds_dwordx4 v[228:229], off
	v_lshl_add_u64 v[228:229], s[40:41], 0, v[132:133]
	s_add_i32 m0, s7, 0xe000
	s_nop 0
	global_load_lds_dwordx4 v[228:229], off
	s_waitcnt vmcnt(8) lgkmcnt(0)
	s_setprio 1
	s_barrier
	v_mfma_f32_16x16x32_bf16 v[126:129], v[142:145], v[176:179], v[126:129]
	v_mfma_f32_16x16x32_bf16 v[122:125], v[150:153], v[176:179], v[122:125]
	v_mfma_f32_16x16x32_bf16 v[118:121], v[142:145], v[204:207], v[118:121]
	v_mfma_f32_16x16x32_bf16 v[114:117], v[150:153], v[204:207], v[114:117]
	v_mfma_f32_16x16x32_bf16 v[106:109], v[142:145], v[212:215], v[106:109]
	v_mfma_f32_16x16x32_bf16 v[98:101], v[150:153], v[212:215], v[98:101]
	v_mfma_f32_16x16x32_bf16 v[90:93], v[142:145], v[220:223], v[90:93]
	v_mfma_f32_16x16x32_bf16 v[82:85], v[150:153], v[220:223], v[82:85]
	v_mfma_f32_16x16x32_bf16 v[126:129], v[146:149], v[200:203], v[126:129]
	v_mfma_f32_16x16x32_bf16 v[122:125], v[154:157], v[200:203], v[122:125]
	v_mfma_f32_16x16x32_bf16 v[118:121], v[146:149], v[208:211], v[118:121]
	v_mfma_f32_16x16x32_bf16 v[114:117], v[154:157], v[208:211], v[114:117]
	v_mfma_f32_16x16x32_bf16 v[106:109], v[146:149], v[216:219], v[106:109]
	v_mfma_f32_16x16x32_bf16 v[98:101], v[154:157], v[216:219], v[98:101]
	v_mfma_f32_16x16x32_bf16 v[90:93], v[146:149], v[224:227], v[90:93]
	v_mfma_f32_16x16x32_bf16 v[82:85], v[154:157], v[224:227], v[82:85]
	s_setprio 0
	s_setprio 1
	v_mfma_f32_16x16x32_bf16 v[110:113], v[158:161], v[176:179], v[110:113]
	v_mfma_f32_16x16x32_bf16 v[102:105], v[168:171], v[176:179], v[102:105]
	v_mfma_f32_16x16x32_bf16 v[94:97], v[158:161], v[204:207], v[94:97]
	v_mfma_f32_16x16x32_bf16 v[86:89], v[168:171], v[204:207], v[86:89]
	v_mfma_f32_16x16x32_bf16 v[78:81], v[158:161], v[212:215], v[78:81]
	v_mfma_f32_16x16x32_bf16 v[74:77], v[168:171], v[212:215], v[74:77]
	v_mfma_f32_16x16x32_bf16 v[70:73], v[158:161], v[220:223], v[70:73]
	v_mfma_f32_16x16x32_bf16 v[66:69], v[168:171], v[220:223], v[66:69]
	v_mfma_f32_16x16x32_bf16 v[110:113], v[164:167], v[200:203], v[110:113]
	v_mfma_f32_16x16x32_bf16 v[102:105], v[172:175], v[200:203], v[102:105]
	v_mfma_f32_16x16x32_bf16 v[94:97], v[164:167], v[208:211], v[94:97]
	v_mfma_f32_16x16x32_bf16 v[86:89], v[172:175], v[208:211], v[86:89]
	v_mfma_f32_16x16x32_bf16 v[78:81], v[164:167], v[216:219], v[78:81]
	v_mfma_f32_16x16x32_bf16 v[74:77], v[172:175], v[216:219], v[74:77]
	v_mfma_f32_16x16x32_bf16 v[70:73], v[164:167], v[224:227], v[70:73]
	v_mfma_f32_16x16x32_bf16 v[66:69], v[172:175], v[224:227], v[66:69]
	s_barrier
	s_setprio 0
	ds_read_b128 v[176:179], v140 offset:16384
	ds_read_b128 v[200:203], v140 offset:17408
	ds_read_b128 v[204:207], v140 offset:18432
	ds_read_b128 v[208:211], v140 offset:19456
	ds_read_b128 v[212:215], v140 offset:20480
	ds_read_b128 v[216:219], v140 offset:21504
	ds_read_b128 v[220:223], v140 offset:22528
	ds_read_b128 v[224:227], v140 offset:23552
	s_add_i32 s40, s44, s31
	v_lshl_add_u64 v[228:229], s[22:23], 0, v[162:163]
	s_mov_b32 m0, s40
	s_nop 0
	global_load_lds_dwordx4 v[228:229], off
	s_add_i32 m0, s40, 0x2000
	s_add_u32 s40, s22, 0x10000
	v_lshl_add_u64 v[230:231], s[22:23], 0, v[134:135]
	s_addc_u32 s41, s23, 0
	s_add_i32 s42, s43, s31
	global_load_lds_dwordx4 v[230:231], off
	v_lshl_add_u64 v[232:233], s[40:41], 0, v[162:163]
	s_mov_b32 m0, s42
	v_lshl_add_u64 v[234:235], s[24:25], 0, v[132:133]
	global_load_lds_dwordx4 v[232:233], off
	v_lshl_add_u64 v[232:233], s[40:41], 0, v[134:135]
	s_add_i32 m0, s42, 0x2000
	s_nop 0
	global_load_lds_dwordx4 v[232:233], off
	v_lshl_add_u64 v[232:233], s[24:25], 0, v[130:131]
	s_mov_b32 m0, s7
	s_nop 0
	global_load_lds_dwordx4 v[232:233], off
	s_mov_b32 m0, s33
	s_nop 0
	global_load_lds_dwordx4 v[234:235], off
	s_waitcnt vmcnt(8) lgkmcnt(0)
	s_setprio 1
	s_barrier
	v_mfma_f32_16x16x32_bf16 v[62:65], v[142:145], v[176:179], v[62:65]
	v_mfma_f32_16x16x32_bf16 v[58:61], v[150:153], v[176:179], v[58:61]
	v_mfma_f32_16x16x32_bf16 v[54:57], v[142:145], v[204:207], v[54:57]
	v_mfma_f32_16x16x32_bf16 v[50:53], v[150:153], v[204:207], v[50:53]
	v_mfma_f32_16x16x32_bf16 v[42:45], v[142:145], v[212:215], v[42:45]
	v_mfma_f32_16x16x32_bf16 v[34:37], v[150:153], v[212:215], v[34:37]
	v_mfma_f32_16x16x32_bf16 v[26:29], v[142:145], v[220:223], v[26:29]
	v_mfma_f32_16x16x32_bf16 v[18:21], v[150:153], v[220:223], v[18:21]
	v_mfma_f32_16x16x32_bf16 v[62:65], v[146:149], v[200:203], v[62:65]
	v_mfma_f32_16x16x32_bf16 v[58:61], v[154:157], v[200:203], v[58:61]
	v_mfma_f32_16x16x32_bf16 v[54:57], v[146:149], v[208:211], v[54:57]
	v_mfma_f32_16x16x32_bf16 v[50:53], v[154:157], v[208:211], v[50:53]
	v_mfma_f32_16x16x32_bf16 v[42:45], v[146:149], v[216:219], v[42:45]
	v_mfma_f32_16x16x32_bf16 v[34:37], v[154:157], v[216:219], v[34:37]
	v_mfma_f32_16x16x32_bf16 v[26:29], v[146:149], v[224:227], v[26:29]
	v_mfma_f32_16x16x32_bf16 v[18:21], v[154:157], v[224:227], v[18:21]
	s_setprio 0
	s_setprio 1
	v_mfma_f32_16x16x32_bf16 v[46:49], v[158:161], v[176:179], v[46:49]
	v_mfma_f32_16x16x32_bf16 v[38:41], v[168:171], v[176:179], v[38:41]
	v_mfma_f32_16x16x32_bf16 v[30:33], v[158:161], v[204:207], v[30:33]
	v_mfma_f32_16x16x32_bf16 v[22:25], v[168:171], v[204:207], v[22:25]
	v_mfma_f32_16x16x32_bf16 v[14:17], v[158:161], v[212:215], v[14:17]
	v_mfma_f32_16x16x32_bf16 v[10:13], v[168:171], v[212:215], v[10:13]
	v_mfma_f32_16x16x32_bf16 v[6:9], v[158:161], v[220:223], v[6:9]
	v_mfma_f32_16x16x32_bf16 v[2:5], v[168:171], v[220:223], v[2:5]
	v_mfma_f32_16x16x32_bf16 v[46:49], v[164:167], v[200:203], v[46:49]
	v_mfma_f32_16x16x32_bf16 v[38:41], v[172:175], v[200:203], v[38:41]
	v_mfma_f32_16x16x32_bf16 v[30:33], v[164:167], v[208:211], v[30:33]
	v_mfma_f32_16x16x32_bf16 v[22:25], v[172:175], v[208:211], v[22:25]
	v_mfma_f32_16x16x32_bf16 v[14:17], v[164:167], v[216:219], v[14:17]
	v_mfma_f32_16x16x32_bf16 v[10:13], v[172:175], v[216:219], v[10:13]
	v_mfma_f32_16x16x32_bf16 v[6:9], v[164:167], v[224:227], v[6:9]
	v_mfma_f32_16x16x32_bf16 v[2:5], v[172:175], v[224:227], v[2:5]
	s_barrier
	s_setprio 0
	s_add_i32 s40, 0, 0x18000
	v_add_u32_e32 v141, s40, v139
	s_add_i32 s41, 0, 0x1c000
	ds_read_b128 v[142:145], v141
	ds_read_b128 v[146:149], v141 offset:1024
	ds_read_b128 v[150:153], v141 offset:2048
	ds_read_b128 v[154:157], v141 offset:3072
	v_add_u32_e32 v141, s41, v139
	ds_read_b128 v[158:161], v141
	ds_read_b128 v[164:167], v141 offset:1024
	ds_read_b128 v[168:171], v141 offset:2048
	ds_read_b128 v[172:175], v141 offset:3072
	ds_read_b128 v[176:179], v140 offset:32768
	ds_read_b128 v[200:203], v140 offset:33792
	ds_read_b128 v[204:207], v140 offset:34816
	ds_read_b128 v[208:211], v140 offset:35840
	ds_read_b128 v[212:215], v140 offset:36864
	ds_read_b128 v[216:219], v140 offset:37888
	ds_read_b128 v[220:223], v140 offset:38912
	ds_read_b128 v[224:227], v140 offset:39936
	s_add_u32 s24, s24, 0x20000
	s_addc_u32 s25, s25, 0
	s_mov_b32 m0, s34
	v_lshl_add_u64 v[236:237], s[24:25], 0, v[130:131]
	global_load_lds_dwordx4 v[236:237], off
	v_lshl_add_u64 v[236:237], s[24:25], 0, v[132:133]
	s_mov_b32 m0, s35
	s_nop 0
	global_load_lds_dwordx4 v[236:237], off
	s_waitcnt vmcnt(8) lgkmcnt(0)
	s_setprio 1
	s_barrier
	v_mfma_f32_16x16x32_bf16 v[126:129], v[142:145], v[176:179], v[126:129]
	v_mfma_f32_16x16x32_bf16 v[122:125], v[150:153], v[176:179], v[122:125]
	v_mfma_f32_16x16x32_bf16 v[118:121], v[142:145], v[204:207], v[118:121]
	v_mfma_f32_16x16x32_bf16 v[114:117], v[150:153], v[204:207], v[114:117]
	v_mfma_f32_16x16x32_bf16 v[106:109], v[142:145], v[212:215], v[106:109]
	v_mfma_f32_16x16x32_bf16 v[98:101], v[150:153], v[212:215], v[98:101]
	v_mfma_f32_16x16x32_bf16 v[90:93], v[142:145], v[220:223], v[90:93]
	v_mfma_f32_16x16x32_bf16 v[82:85], v[150:153], v[220:223], v[82:85]
	v_mfma_f32_16x16x32_bf16 v[126:129], v[146:149], v[200:203], v[126:129]
	v_mfma_f32_16x16x32_bf16 v[122:125], v[154:157], v[200:203], v[122:125]
	v_mfma_f32_16x16x32_bf16 v[118:121], v[146:149], v[208:211], v[118:121]
	v_mfma_f32_16x16x32_bf16 v[114:117], v[154:157], v[208:211], v[114:117]
	v_mfma_f32_16x16x32_bf16 v[106:109], v[146:149], v[216:219], v[106:109]
	v_mfma_f32_16x16x32_bf16 v[98:101], v[154:157], v[216:219], v[98:101]
	v_mfma_f32_16x16x32_bf16 v[90:93], v[146:149], v[224:227], v[90:93]
	v_mfma_f32_16x16x32_bf16 v[82:85], v[154:157], v[224:227], v[82:85]
	s_setprio 0
	s_setprio 1
	v_mfma_f32_16x16x32_bf16 v[110:113], v[158:161], v[176:179], v[110:113]
	v_mfma_f32_16x16x32_bf16 v[102:105], v[168:171], v[176:179], v[102:105]
	v_mfma_f32_16x16x32_bf16 v[94:97], v[158:161], v[204:207], v[94:97]
	v_mfma_f32_16x16x32_bf16 v[86:89], v[168:171], v[204:207], v[86:89]
	v_mfma_f32_16x16x32_bf16 v[78:81], v[158:161], v[212:215], v[78:81]
	v_mfma_f32_16x16x32_bf16 v[74:77], v[168:171], v[212:215], v[74:77]
	v_mfma_f32_16x16x32_bf16 v[70:73], v[158:161], v[220:223], v[70:73]
	v_mfma_f32_16x16x32_bf16 v[66:69], v[168:171], v[220:223], v[66:69]
	v_mfma_f32_16x16x32_bf16 v[110:113], v[164:167], v[200:203], v[110:113]
	v_mfma_f32_16x16x32_bf16 v[102:105], v[172:175], v[200:203], v[102:105]
	v_mfma_f32_16x16x32_bf16 v[94:97], v[164:167], v[208:211], v[94:97]
	v_mfma_f32_16x16x32_bf16 v[86:89], v[172:175], v[208:211], v[86:89]
	v_mfma_f32_16x16x32_bf16 v[78:81], v[164:167], v[216:219], v[78:81]
	v_mfma_f32_16x16x32_bf16 v[74:77], v[172:175], v[216:219], v[74:77]
	v_mfma_f32_16x16x32_bf16 v[70:73], v[164:167], v[224:227], v[70:73]
	v_mfma_f32_16x16x32_bf16 v[66:69], v[172:175], v[224:227], v[66:69]
	s_barrier
	s_setprio 0
	ds_read_b128 v[176:179], v140 offset:49152
	ds_read_b128 v[200:203], v140 offset:50176
	ds_read_b128 v[204:207], v140 offset:51200
	ds_read_b128 v[208:211], v140 offset:52224
	ds_read_b128 v[212:215], v140 offset:53248
	ds_read_b128 v[216:219], v140 offset:54272
	ds_read_b128 v[220:223], v140 offset:55296
	ds_read_b128 v[224:227], v140 offset:56320
	s_add_i32 s24, s40, s31
	v_lshl_add_u64 v[228:229], v[228:229], 0, s[90:91]
	s_mov_b32 m0, s24
	s_nop 0
	global_load_lds_dwordx4 v[228:229], off
	s_add_i32 m0, s24, 0x2000
	s_add_u32 s22, s22, 0x10080
	v_lshl_add_u64 v[228:229], v[230:231], 0, s[90:91]
	s_addc_u32 s23, s23, 0
	s_add_i32 s24, s41, s31
	global_load_lds_dwordx4 v[228:229], off
	v_lshl_add_u64 v[228:229], s[22:23], 0, v[162:163]
	s_mov_b32 m0, s24
	s_nop 0
	global_load_lds_dwordx4 v[228:229], off
	v_lshl_add_u64 v[228:229], s[22:23], 0, v[134:135]
	s_add_i32 m0, s24, 0x2000
	s_nop 0
	global_load_lds_dwordx4 v[228:229], off
	v_lshl_add_u64 v[228:229], v[232:233], 0, s[90:91]
	s_mov_b32 m0, s36
	s_nop 0
	global_load_lds_dwordx4 v[228:229], off
	v_lshl_add_u64 v[228:229], v[234:235], 0, s[90:91]
	s_mov_b32 m0, s37
	s_nop 0
	global_load_lds_dwordx4 v[228:229], off
	s_waitcnt vmcnt(8) lgkmcnt(0)
	s_setprio 1
	s_barrier
	v_mfma_f32_16x16x32_bf16 v[62:65], v[142:145], v[176:179], v[62:65]
	v_mfma_f32_16x16x32_bf16 v[58:61], v[150:153], v[176:179], v[58:61]
	v_mfma_f32_16x16x32_bf16 v[54:57], v[142:145], v[204:207], v[54:57]
	v_mfma_f32_16x16x32_bf16 v[50:53], v[150:153], v[204:207], v[50:53]
	v_mfma_f32_16x16x32_bf16 v[42:45], v[142:145], v[212:215], v[42:45]
	v_mfma_f32_16x16x32_bf16 v[34:37], v[150:153], v[212:215], v[34:37]
	v_mfma_f32_16x16x32_bf16 v[26:29], v[142:145], v[220:223], v[26:29]
	v_mfma_f32_16x16x32_bf16 v[18:21], v[150:153], v[220:223], v[18:21]
	v_mfma_f32_16x16x32_bf16 v[62:65], v[146:149], v[200:203], v[62:65]
	v_mfma_f32_16x16x32_bf16 v[58:61], v[154:157], v[200:203], v[58:61]
	v_mfma_f32_16x16x32_bf16 v[54:57], v[146:149], v[208:211], v[54:57]
	v_mfma_f32_16x16x32_bf16 v[50:53], v[154:157], v[208:211], v[50:53]
	v_mfma_f32_16x16x32_bf16 v[42:45], v[146:149], v[216:219], v[42:45]
	v_mfma_f32_16x16x32_bf16 v[34:37], v[154:157], v[216:219], v[34:37]
	v_mfma_f32_16x16x32_bf16 v[26:29], v[146:149], v[224:227], v[26:29]
	v_mfma_f32_16x16x32_bf16 v[18:21], v[154:157], v[224:227], v[18:21]
	s_setprio 0
	s_setprio 1
	v_mfma_f32_16x16x32_bf16 v[46:49], v[158:161], v[176:179], v[46:49]
	v_mfma_f32_16x16x32_bf16 v[38:41], v[168:171], v[176:179], v[38:41]
	v_mfma_f32_16x16x32_bf16 v[30:33], v[158:161], v[204:207], v[30:33]
	v_mfma_f32_16x16x32_bf16 v[22:25], v[168:171], v[204:207], v[22:25]
	v_mfma_f32_16x16x32_bf16 v[14:17], v[158:161], v[212:215], v[14:17]
	v_mfma_f32_16x16x32_bf16 v[10:13], v[168:171], v[212:215], v[10:13]
	v_mfma_f32_16x16x32_bf16 v[6:9], v[158:161], v[220:223], v[6:9]
	v_mfma_f32_16x16x32_bf16 v[2:5], v[168:171], v[220:223], v[2:5]
	v_mfma_f32_16x16x32_bf16 v[46:49], v[164:167], v[200:203], v[46:49]
	v_mfma_f32_16x16x32_bf16 v[38:41], v[172:175], v[200:203], v[38:41]
	v_mfma_f32_16x16x32_bf16 v[30:33], v[164:167], v[208:211], v[30:33]
	v_mfma_f32_16x16x32_bf16 v[22:25], v[172:175], v[208:211], v[22:25]
	v_mfma_f32_16x16x32_bf16 v[14:17], v[164:167], v[216:219], v[14:17]
	v_mfma_f32_16x16x32_bf16 v[10:13], v[172:175], v[216:219], v[10:13]
	v_mfma_f32_16x16x32_bf16 v[6:9], v[164:167], v[224:227], v[6:9]
	v_mfma_f32_16x16x32_bf16 v[2:5], v[172:175], v[224:227], v[2:5]
	s_barrier
	s_setprio 0
	s_movk_i32 s40, 0x100
	s_and_b64 vcc, exec, s[20:21]
	s_mov_b64 s[22:23], -1
	s_mov_b64 s[20:21], 0
	s_cbranch_vccnz .LBB0_318
	s_andn2_b64 vcc, exec, s[12:13]
	s_cbranch_vccnz .LBB0_321
	s_barrier

.LBB0_775:
	s_add_i32 s42, 0, 0x10000
	v_add_u32_e32 v139, s42, v141
	s_add_i32 s44, 0, 0x14000
	ds_read_b128 v[146:149], v139
	ds_read_b128 v[150:153], v139 offset:1024
	ds_read_b128 v[154:157], v139 offset:2048
	ds_read_b128 v[158:161], v139 offset:3072
	v_add_u32_e32 v139, s44, v141
	ds_read_b128 v[164:167], v139
	ds_read_b128 v[172:175], v139 offset:1024
	ds_read_b128 v[176:179], v139 offset:2048
	ds_read_b128 v[200:203], v139 offset:3072
	ds_read_b128 v[204:207], v144
	ds_read_b128 v[208:211], v144 offset:1024
	ds_read_b128 v[212:215], v144 offset:2048
	ds_read_b128 v[216:219], v144 offset:3072
	ds_read_b128 v[220:223], v144 offset:4096
	ds_read_b128 v[224:227], v144 offset:5120
	ds_read_b128 v[228:231], v144 offset:6144
	ds_read_b128 v[232:235], v144 offset:7168
	s_add_u32 s20, s18, 0xfffe0080
	s_addc_u32 s21, s19, -1
	s_cmp_eq_u32 s41, 4
	s_cselect_b32 s23, s11, s21
	s_cselect_b32 s22, s17, s20
	s_cselect_b32 s21, s13, s40
	s_cselect_b32 s20, s12, s33
	v_lshl_add_u64 v[168:169], s[18:19], 0, v[136:137]
	s_add_i32 m0, s30, 0xc000
	s_nop 0
	global_load_lds_dwordx4 v[168:169], off
	v_lshl_add_u64 v[168:169], s[18:19], 0, v[134:135]
	s_add_i32 m0, s30, 0xe000
	s_nop 0
	global_load_lds_dwordx4 v[168:169], off
	s_waitcnt vmcnt(8) lgkmcnt(0)
	s_setprio 1
	s_barrier
	v_mfma_f32_16x16x32_bf16 v[126:129], v[146:149], v[204:207], v[126:129]
	v_mfma_f32_16x16x32_bf16 v[122:125], v[154:157], v[204:207], v[122:125]
	v_mfma_f32_16x16x32_bf16 v[110:113], v[146:149], v[212:215], v[110:113]
	v_mfma_f32_16x16x32_bf16 v[106:109], v[154:157], v[212:215], v[106:109]
	v_mfma_f32_16x16x32_bf16 v[94:97], v[146:149], v[220:223], v[94:97]
	v_mfma_f32_16x16x32_bf16 v[90:93], v[154:157], v[220:223], v[90:93]
	v_mfma_f32_16x16x32_bf16 v[78:81], v[146:149], v[228:231], v[78:81]
	v_mfma_f32_16x16x32_bf16 v[74:77], v[154:157], v[228:231], v[74:77]
	v_mfma_f32_16x16x32_bf16 v[126:129], v[150:153], v[208:211], v[126:129]
	v_mfma_f32_16x16x32_bf16 v[122:125], v[158:161], v[208:211], v[122:125]
	v_mfma_f32_16x16x32_bf16 v[110:113], v[150:153], v[216:219], v[110:113]
	v_mfma_f32_16x16x32_bf16 v[106:109], v[158:161], v[216:219], v[106:109]
	v_mfma_f32_16x16x32_bf16 v[94:97], v[150:153], v[224:227], v[94:97]
	v_mfma_f32_16x16x32_bf16 v[90:93], v[158:161], v[224:227], v[90:93]
	v_mfma_f32_16x16x32_bf16 v[78:81], v[150:153], v[232:235], v[78:81]
	v_mfma_f32_16x16x32_bf16 v[74:77], v[158:161], v[232:235], v[74:77]
	s_setprio 0
	s_setprio 1
	v_mfma_f32_16x16x32_bf16 v[118:121], v[164:167], v[204:207], v[118:121]
	v_mfma_f32_16x16x32_bf16 v[114:117], v[176:179], v[204:207], v[114:117]
	v_mfma_f32_16x16x32_bf16 v[102:105], v[164:167], v[212:215], v[102:105]
	v_mfma_f32_16x16x32_bf16 v[98:101], v[176:179], v[212:215], v[98:101]
	v_mfma_f32_16x16x32_bf16 v[86:89], v[164:167], v[220:223], v[86:89]
	v_mfma_f32_16x16x32_bf16 v[82:85], v[176:179], v[220:223], v[82:85]
	v_mfma_f32_16x16x32_bf16 v[70:73], v[164:167], v[228:231], v[70:73]
	v_mfma_f32_16x16x32_bf16 v[66:69], v[176:179], v[228:231], v[66:69]
	v_mfma_f32_16x16x32_bf16 v[118:121], v[172:175], v[208:211], v[118:121]
	v_mfma_f32_16x16x32_bf16 v[114:117], v[200:203], v[208:211], v[114:117]
	v_mfma_f32_16x16x32_bf16 v[102:105], v[172:175], v[216:219], v[102:105]
	v_mfma_f32_16x16x32_bf16 v[98:101], v[200:203], v[216:219], v[98:101]
	v_mfma_f32_16x16x32_bf16 v[86:89], v[172:175], v[224:227], v[86:89]
	v_mfma_f32_16x16x32_bf16 v[82:85], v[200:203], v[224:227], v[82:85]
	v_mfma_f32_16x16x32_bf16 v[70:73], v[172:175], v[232:235], v[70:73]
	v_mfma_f32_16x16x32_bf16 v[66:69], v[200:203], v[232:235], v[66:69]
	s_barrier
	s_setprio 0
	ds_read_b128 v[204:207], v144 offset:16384
	ds_read_b128 v[208:211], v144 offset:17408
	ds_read_b128 v[212:215], v144 offset:18432
	ds_read_b128 v[216:219], v144 offset:19456
	ds_read_b128 v[220:223], v144 offset:20480
	ds_read_b128 v[224:227], v144 offset:21504
	ds_read_b128 v[228:231], v144 offset:22528
	ds_read_b128 v[232:235], v144 offset:23552
	s_add_i32 s42, s42, s29
	v_lshl_add_u64 v[168:169], s[20:21], 0, v[130:131]
	s_mov_b32 m0, s42
	s_nop 0
	global_load_lds_dwordx4 v[168:169], off
	s_add_i32 m0, s42, 0x2000
	s_add_u32 s42, s20, 0x20000
	v_lshl_add_u64 v[236:237], s[20:21], 0, v[132:133]
	s_addc_u32 s43, s21, 0
	s_add_i32 s44, s44, s29
	global_load_lds_dwordx4 v[236:237], off
	v_lshl_add_u64 v[238:239], s[42:43], 0, v[130:131]
	s_mov_b32 m0, s44
	v_lshl_add_u64 v[240:241], s[22:23], 0, v[132:133]
	global_load_lds_dwordx4 v[238:239], off
	v_lshl_add_u64 v[238:239], s[42:43], 0, v[132:133]
	s_add_i32 m0, s44, 0x2000
	s_nop 0
	global_load_lds_dwordx4 v[238:239], off
	v_lshl_add_u64 v[238:239], s[22:23], 0, v[130:131]
	s_mov_b32 m0, s30
	s_nop 0
	global_load_lds_dwordx4 v[238:239], off
	s_mov_b32 m0, s31
	s_nop 0
	global_load_lds_dwordx4 v[240:241], off
	s_waitcnt vmcnt(8) lgkmcnt(0)
	s_setprio 1
	s_barrier
	v_mfma_f32_16x16x32_bf16 v[62:65], v[146:149], v[204:207], v[62:65]
	v_mfma_f32_16x16x32_bf16 v[58:61], v[154:157], v[204:207], v[58:61]
	v_mfma_f32_16x16x32_bf16 v[46:49], v[146:149], v[212:215], v[46:49]
	v_mfma_f32_16x16x32_bf16 v[42:45], v[154:157], v[212:215], v[42:45]
	v_mfma_f32_16x16x32_bf16 v[30:33], v[146:149], v[220:223], v[30:33]
	v_mfma_f32_16x16x32_bf16 v[26:29], v[154:157], v[220:223], v[26:29]
	v_mfma_f32_16x16x32_bf16 v[14:17], v[146:149], v[228:231], v[14:17]
	v_mfma_f32_16x16x32_bf16 v[10:13], v[154:157], v[228:231], v[10:13]
	v_mfma_f32_16x16x32_bf16 v[62:65], v[150:153], v[208:211], v[62:65]
	v_mfma_f32_16x16x32_bf16 v[58:61], v[158:161], v[208:211], v[58:61]
	v_mfma_f32_16x16x32_bf16 v[46:49], v[150:153], v[216:219], v[46:49]
	v_mfma_f32_16x16x32_bf16 v[42:45], v[158:161], v[216:219], v[42:45]
	v_mfma_f32_16x16x32_bf16 v[30:33], v[150:153], v[224:227], v[30:33]
	v_mfma_f32_16x16x32_bf16 v[26:29], v[158:161], v[224:227], v[26:29]
	v_mfma_f32_16x16x32_bf16 v[14:17], v[150:153], v[232:235], v[14:17]
	v_mfma_f32_16x16x32_bf16 v[10:13], v[158:161], v[232:235], v[10:13]
	s_setprio 0
	s_setprio 1
	v_mfma_f32_16x16x32_bf16 v[54:57], v[164:167], v[204:207], v[54:57]
	v_mfma_f32_16x16x32_bf16 v[50:53], v[176:179], v[204:207], v[50:53]
	v_mfma_f32_16x16x32_bf16 v[38:41], v[164:167], v[212:215], v[38:41]
	v_mfma_f32_16x16x32_bf16 v[34:37], v[176:179], v[212:215], v[34:37]
	v_mfma_f32_16x16x32_bf16 v[22:25], v[164:167], v[220:223], v[22:25]
	v_mfma_f32_16x16x32_bf16 v[18:21], v[176:179], v[220:223], v[18:21]
	v_mfma_f32_16x16x32_bf16 v[6:9], v[164:167], v[228:231], v[6:9]
	v_mfma_f32_16x16x32_bf16 v[2:5], v[176:179], v[228:231], v[2:5]
	v_mfma_f32_16x16x32_bf16 v[54:57], v[172:175], v[208:211], v[54:57]
	v_mfma_f32_16x16x32_bf16 v[50:53], v[200:203], v[208:211], v[50:53]
	v_mfma_f32_16x16x32_bf16 v[38:41], v[172:175], v[216:219], v[38:41]
	v_mfma_f32_16x16x32_bf16 v[34:37], v[200:203], v[216:219], v[34:37]
	v_mfma_f32_16x16x32_bf16 v[22:25], v[172:175], v[224:227], v[22:25]
	v_mfma_f32_16x16x32_bf16 v[18:21], v[200:203], v[224:227], v[18:21]
	v_mfma_f32_16x16x32_bf16 v[6:9], v[172:175], v[232:235], v[6:9]
	v_mfma_f32_16x16x32_bf16 v[2:5], v[200:203], v[232:235], v[2:5]
	s_barrier
	s_setprio 0
	s_add_i32 s42, 0, 0x18000
	v_add_u32_e32 v139, s42, v141
	s_add_i32 s43, 0, 0x1c000
	ds_read_b128 v[146:149], v139
	ds_read_b128 v[150:153], v139 offset:1024
	ds_read_b128 v[154:157], v139 offset:2048
	ds_read_b128 v[158:161], v139 offset:3072
	v_add_u32_e32 v139, s43, v141
	ds_read_b128 v[164:167], v139
	ds_read_b128 v[172:175], v139 offset:1024
	ds_read_b128 v[176:179], v139 offset:2048
	ds_read_b128 v[200:203], v139 offset:3072
	ds_read_b128 v[204:207], v144 offset:32768
	ds_read_b128 v[208:211], v144 offset:33792
	ds_read_b128 v[212:215], v144 offset:34816
	ds_read_b128 v[216:219], v144 offset:35840
	ds_read_b128 v[220:223], v144 offset:36864
	ds_read_b128 v[224:227], v144 offset:37888
	ds_read_b128 v[228:231], v144 offset:38912
	ds_read_b128 v[232:235], v144 offset:39936
	s_add_u32 s22, s22, 0x20000
	s_addc_u32 s23, s23, 0
	s_mov_b32 m0, s34
	v_lshl_add_u64 v[242:243], s[22:23], 0, v[130:131]
	global_load_lds_dwordx4 v[242:243], off
	v_lshl_add_u64 v[242:243], s[22:23], 0, v[132:133]
	s_mov_b32 m0, s35
	s_nop 0
	global_load_lds_dwordx4 v[242:243], off
	s_waitcnt vmcnt(8) lgkmcnt(0)
	s_setprio 1
	s_barrier
	v_mfma_f32_16x16x32_bf16 v[126:129], v[146:149], v[204:207], v[126:129]
	v_mfma_f32_16x16x32_bf16 v[122:125], v[154:157], v[204:207], v[122:125]
	v_mfma_f32_16x16x32_bf16 v[110:113], v[146:149], v[212:215], v[110:113]
	v_mfma_f32_16x16x32_bf16 v[106:109], v[154:157], v[212:215], v[106:109]
	v_mfma_f32_16x16x32_bf16 v[94:97], v[146:149], v[220:223], v[94:97]
	v_mfma_f32_16x16x32_bf16 v[90:93], v[154:157], v[220:223], v[90:93]
	v_mfma_f32_16x16x32_bf16 v[78:81], v[146:149], v[228:231], v[78:81]
	v_mfma_f32_16x16x32_bf16 v[74:77], v[154:157], v[228:231], v[74:77]
	v_mfma_f32_16x16x32_bf16 v[126:129], v[150:153], v[208:211], v[126:129]
	v_mfma_f32_16x16x32_bf16 v[122:125], v[158:161], v[208:211], v[122:125]
	v_mfma_f32_16x16x32_bf16 v[110:113], v[150:153], v[216:219], v[110:113]
	v_mfma_f32_16x16x32_bf16 v[106:109], v[158:161], v[216:219], v[106:109]
	v_mfma_f32_16x16x32_bf16 v[94:97], v[150:153], v[224:227], v[94:97]
	v_mfma_f32_16x16x32_bf16 v[90:93], v[158:161], v[224:227], v[90:93]
	v_mfma_f32_16x16x32_bf16 v[78:81], v[150:153], v[232:235], v[78:81]
	v_mfma_f32_16x16x32_bf16 v[74:77], v[158:161], v[232:235], v[74:77]
	s_setprio 0
	s_setprio 1
	v_mfma_f32_16x16x32_bf16 v[118:121], v[164:167], v[204:207], v[118:121]
	v_mfma_f32_16x16x32_bf16 v[114:117], v[176:179], v[204:207], v[114:117]
	v_mfma_f32_16x16x32_bf16 v[102:105], v[164:167], v[212:215], v[102:105]
	v_mfma_f32_16x16x32_bf16 v[98:101], v[176:179], v[212:215], v[98:101]
	v_mfma_f32_16x16x32_bf16 v[86:89], v[164:167], v[220:223], v[86:89]
	v_mfma_f32_16x16x32_bf16 v[82:85], v[176:179], v[220:223], v[82:85]
	v_mfma_f32_16x16x32_bf16 v[70:73], v[164:167], v[228:231], v[70:73]
	v_mfma_f32_16x16x32_bf16 v[66:69], v[176:179], v[228:231], v[66:69]
	v_mfma_f32_16x16x32_bf16 v[118:121], v[172:175], v[208:211], v[118:121]
	v_mfma_f32_16x16x32_bf16 v[114:117], v[200:203], v[208:211], v[114:117]
	v_mfma_f32_16x16x32_bf16 v[102:105], v[172:175], v[216:219], v[102:105]
	v_mfma_f32_16x16x32_bf16 v[98:101], v[200:203], v[216:219], v[98:101]
	v_mfma_f32_16x16x32_bf16 v[86:89], v[172:175], v[224:227], v[86:89]
	v_mfma_f32_16x16x32_bf16 v[82:85], v[200:203], v[224:227], v[82:85]
	v_mfma_f32_16x16x32_bf16 v[70:73], v[172:175], v[232:235], v[70:73]
	v_mfma_f32_16x16x32_bf16 v[66:69], v[200:203], v[232:235], v[66:69]
	s_barrier
	s_setprio 0
	ds_read_b128 v[204:207], v144 offset:49152
	ds_read_b128 v[208:211], v144 offset:50176
	ds_read_b128 v[212:215], v144 offset:51200
	ds_read_b128 v[216:219], v144 offset:52224
	ds_read_b128 v[220:223], v144 offset:53248
	ds_read_b128 v[224:227], v144 offset:54272
	ds_read_b128 v[228:231], v144 offset:55296
	ds_read_b128 v[232:235], v144 offset:56320
	s_add_i32 s22, s42, s29
	v_lshl_add_u64 v[168:169], v[168:169], 0, s[90:91]
	s_mov_b32 m0, s22
	s_nop 0
	global_load_lds_dwordx4 v[168:169], off
	s_add_i32 m0, s22, 0x2000
	s_add_u32 s20, s20, 0x20080
	v_lshl_add_u64 v[168:169], v[236:237], 0, s[90:91]
	s_addc_u32 s21, s21, 0
	s_add_i32 s22, s43, s29
	global_load_lds_dwordx4 v[168:169], off
	v_lshl_add_u64 v[168:169], s[20:21], 0, v[130:131]
	s_mov_b32 m0, s22
	s_nop 0
	global_load_lds_dwordx4 v[168:169], off
	v_lshl_add_u64 v[168:169], s[20:21], 0, v[132:133]
	s_add_i32 m0, s22, 0x2000
	s_nop 0
	global_load_lds_dwordx4 v[168:169], off
	v_lshl_add_u64 v[168:169], v[238:239], 0, s[90:91]
	s_mov_b32 m0, s37
	s_nop 0
	global_load_lds_dwordx4 v[168:169], off
	v_lshl_add_u64 v[168:169], v[240:241], 0, s[90:91]
	s_mov_b32 m0, s38
	s_nop 0
	global_load_lds_dwordx4 v[168:169], off
	s_waitcnt vmcnt(8) lgkmcnt(0)
	s_setprio 1
	s_barrier
	v_mfma_f32_16x16x32_bf16 v[62:65], v[146:149], v[204:207], v[62:65]
	v_mfma_f32_16x16x32_bf16 v[58:61], v[154:157], v[204:207], v[58:61]
	v_mfma_f32_16x16x32_bf16 v[46:49], v[146:149], v[212:215], v[46:49]
	v_mfma_f32_16x16x32_bf16 v[42:45], v[154:157], v[212:215], v[42:45]
	v_mfma_f32_16x16x32_bf16 v[30:33], v[146:149], v[220:223], v[30:33]
	v_mfma_f32_16x16x32_bf16 v[26:29], v[154:157], v[220:223], v[26:29]
	v_mfma_f32_16x16x32_bf16 v[14:17], v[146:149], v[228:231], v[14:17]
	v_mfma_f32_16x16x32_bf16 v[10:13], v[154:157], v[228:231], v[10:13]
	v_mfma_f32_16x16x32_bf16 v[62:65], v[150:153], v[208:211], v[62:65]
	v_mfma_f32_16x16x32_bf16 v[58:61], v[158:161], v[208:211], v[58:61]
	v_mfma_f32_16x16x32_bf16 v[46:49], v[150:153], v[216:219], v[46:49]
	v_mfma_f32_16x16x32_bf16 v[42:45], v[158:161], v[216:219], v[42:45]
	v_mfma_f32_16x16x32_bf16 v[30:33], v[150:153], v[224:227], v[30:33]
	v_mfma_f32_16x16x32_bf16 v[26:29], v[158:161], v[224:227], v[26:29]
	v_mfma_f32_16x16x32_bf16 v[14:17], v[150:153], v[232:235], v[14:17]
	v_mfma_f32_16x16x32_bf16 v[10:13], v[158:161], v[232:235], v[10:13]
	s_setprio 0
	s_setprio 1
	v_mfma_f32_16x16x32_bf16 v[54:57], v[164:167], v[204:207], v[54:57]
	v_mfma_f32_16x16x32_bf16 v[50:53], v[176:179], v[204:207], v[50:53]
	v_mfma_f32_16x16x32_bf16 v[38:41], v[164:167], v[212:215], v[38:41]
	v_mfma_f32_16x16x32_bf16 v[34:37], v[176:179], v[212:215], v[34:37]
	v_mfma_f32_16x16x32_bf16 v[22:25], v[164:167], v[220:223], v[22:25]
	v_mfma_f32_16x16x32_bf16 v[18:21], v[176:179], v[220:223], v[18:21]
	v_mfma_f32_16x16x32_bf16 v[6:9], v[164:167], v[228:231], v[6:9]
	v_mfma_f32_16x16x32_bf16 v[2:5], v[176:179], v[228:231], v[2:5]
	v_mfma_f32_16x16x32_bf16 v[54:57], v[172:175], v[208:211], v[54:57]
	v_mfma_f32_16x16x32_bf16 v[50:53], v[200:203], v[208:211], v[50:53]
	v_mfma_f32_16x16x32_bf16 v[38:41], v[172:175], v[216:219], v[38:41]
	v_mfma_f32_16x16x32_bf16 v[34:37], v[200:203], v[216:219], v[34:37]
	v_mfma_f32_16x16x32_bf16 v[22:25], v[172:175], v[224:227], v[22:25]
	v_mfma_f32_16x16x32_bf16 v[18:21], v[200:203], v[224:227], v[18:21]
	v_mfma_f32_16x16x32_bf16 v[6:9], v[172:175], v[232:235], v[6:9]
	v_mfma_f32_16x16x32_bf16 v[2:5], v[200:203], v[232:235], v[2:5]
	s_barrier
	s_setprio 0
	s_add_i32 s41, s41, 2
	s_add_u32 s33, s33, 0x100
	s_addc_u32 s40, s40, 0
	s_add_u32 s18, s18, 0x100
	s_addc_u32 s19, s19, 0
	s_cmp_lt_u32 s41, 6
	s_cbranch_scc1 .LBB0_775
	s_andn2_b64 vcc, exec, s[8:9]
	s_cbranch_vccnz .LBB0_778
	s_barrier

.LBB0_843:
	s_add_i32 s33, s26, 0x100
	s_add_u32 s41, s20, s26
	s_addc_u32 s43, s21, 0
	s_add_u32 s42, s41, 0x100
	s_addc_u32 s44, s43, 0
	s_and_b64 s[26:27], s[24:25], exec
	s_cselect_b32 s27, s13, s44
	s_cselect_b32 s26, s19, s42
	s_add_i32 s44, 0, 0x10000
	s_and_b64 s[24:25], s[24:25], exec
	s_cselect_b32 s24, 0, s33
	s_cselect_b32 s25, 0, 0
	s_add_u32 s24, s0, s24
	s_addc_u32 s25, s1, s25
	s_add_i32 s33, 0, 0x14000
	v_add_u32_e32 v134, s44, v172
	v_add_u32_e32 v158, s33, v172
	ds_read_b128 v[102:105], v134
	ds_read_b128 v[114:117], v134 offset:1024
	ds_read_b128 v[126:129], v134 offset:2048
	ds_read_b128 v[134:137], v134 offset:3072
	ds_read_b128 v[138:141], v158
	ds_read_b128 v[146:149], v158 offset:1024
	ds_read_b128 v[154:157], v158 offset:2048
	ds_read_b128 v[158:161], v158 offset:3072
	s_add_u32 s42, s41, 0x10080
	s_addc_u32 s43, s43, 0
	v_lshl_add_u64 v[224:225], s[42:43], 0, v[162:163]
	s_add_i32 m0, s34, 0xc000
	ds_read_b128 v[166:169], v173
	ds_read_b128 v[176:179], v173 offset:1024
	ds_read_b128 v[200:203], v173 offset:2048
	ds_read_b128 v[204:207], v173 offset:3072
	ds_read_b128 v[208:211], v173 offset:4096
	ds_read_b128 v[212:215], v173 offset:5120
	ds_read_b128 v[216:219], v173 offset:6144
	ds_read_b128 v[220:223], v173 offset:7168
	global_load_lds_dwordx4 v[224:225], off
	v_lshl_add_u64 v[224:225], s[42:43], 0, v[164:165]
	s_add_i32 m0, s34, 0xe000
	s_nop 0
	global_load_lds_dwordx4 v[224:225], off
	s_waitcnt vmcnt(8) lgkmcnt(0)
	s_setprio 1
	s_barrier
	v_mfma_f32_16x16x32_bf16 v[150:153], v[102:105], v[166:169], v[150:153]
	v_mfma_f32_16x16x32_bf16 v[142:145], v[126:129], v[166:169], v[142:145]
	v_mfma_f32_16x16x32_bf16 v[118:121], v[102:105], v[200:203], v[118:121]
	v_mfma_f32_16x16x32_bf16 v[110:113], v[126:129], v[200:203], v[110:113]
	v_mfma_f32_16x16x32_bf16 v[94:97], v[102:105], v[208:211], v[94:97]
	v_mfma_f32_16x16x32_bf16 v[90:93], v[126:129], v[208:211], v[90:93]
	v_mfma_f32_16x16x32_bf16 v[78:81], v[102:105], v[216:219], v[78:81]
	v_mfma_f32_16x16x32_bf16 v[74:77], v[126:129], v[216:219], v[74:77]
	v_mfma_f32_16x16x32_bf16 v[150:153], v[114:117], v[176:179], v[150:153]
	v_mfma_f32_16x16x32_bf16 v[142:145], v[134:137], v[176:179], v[142:145]
	v_mfma_f32_16x16x32_bf16 v[118:121], v[114:117], v[204:207], v[118:121]
	v_mfma_f32_16x16x32_bf16 v[110:113], v[134:137], v[204:207], v[110:113]
	v_mfma_f32_16x16x32_bf16 v[94:97], v[114:117], v[212:215], v[94:97]
	v_mfma_f32_16x16x32_bf16 v[90:93], v[134:137], v[212:215], v[90:93]
	v_mfma_f32_16x16x32_bf16 v[78:81], v[114:117], v[220:223], v[78:81]
	v_mfma_f32_16x16x32_bf16 v[74:77], v[134:137], v[220:223], v[74:77]
	s_setprio 0
	s_setprio 1
	v_mfma_f32_16x16x32_bf16 v[130:133], v[138:141], v[166:169], v[130:133]
	v_mfma_f32_16x16x32_bf16 v[122:125], v[154:157], v[166:169], v[122:125]
	v_mfma_f32_16x16x32_bf16 v[106:109], v[138:141], v[200:203], v[106:109]
	v_mfma_f32_16x16x32_bf16 v[98:101], v[154:157], v[200:203], v[98:101]
	v_mfma_f32_16x16x32_bf16 v[86:89], v[138:141], v[208:211], v[86:89]
	v_mfma_f32_16x16x32_bf16 v[82:85], v[154:157], v[208:211], v[82:85]
	v_mfma_f32_16x16x32_bf16 v[70:73], v[138:141], v[216:219], v[70:73]
	v_mfma_f32_16x16x32_bf16 v[66:69], v[154:157], v[216:219], v[66:69]
	v_mfma_f32_16x16x32_bf16 v[130:133], v[146:149], v[176:179], v[130:133]
	v_mfma_f32_16x16x32_bf16 v[122:125], v[158:161], v[176:179], v[122:125]
	v_mfma_f32_16x16x32_bf16 v[106:109], v[146:149], v[204:207], v[106:109]
	v_mfma_f32_16x16x32_bf16 v[98:101], v[158:161], v[204:207], v[98:101]
	v_mfma_f32_16x16x32_bf16 v[86:89], v[146:149], v[212:215], v[86:89]
	v_mfma_f32_16x16x32_bf16 v[82:85], v[158:161], v[212:215], v[82:85]
	v_mfma_f32_16x16x32_bf16 v[70:73], v[146:149], v[220:223], v[70:73]
	v_mfma_f32_16x16x32_bf16 v[66:69], v[158:161], v[220:223], v[66:69]
	s_barrier
	s_setprio 0
	ds_read_b128 v[166:169], v173 offset:16384
	ds_read_b128 v[176:179], v173 offset:17408
	ds_read_b128 v[200:203], v173 offset:18432
	ds_read_b128 v[204:207], v173 offset:19456
	ds_read_b128 v[208:211], v173 offset:20480
	ds_read_b128 v[212:215], v173 offset:21504
	ds_read_b128 v[216:219], v173 offset:22528
	ds_read_b128 v[220:223], v173 offset:23552
	s_add_i32 s41, s44, s31
	v_lshl_add_u64 v[224:225], s[24:25], 0, v[162:163]
	s_mov_b32 m0, s41
	s_nop 0
	global_load_lds_dwordx4 v[224:225], off
	s_add_i32 m0, s41, 0x2000
	s_add_u32 s42, s24, 0x10000
	v_lshl_add_u64 v[226:227], s[24:25], 0, v[164:165]
	s_addc_u32 s43, s25, 0
	s_add_i32 s33, s33, s31
	global_load_lds_dwordx4 v[226:227], off
	v_lshl_add_u64 v[228:229], s[42:43], 0, v[162:163]
	s_mov_b32 m0, s33
	v_lshl_add_u64 v[230:231], s[26:27], 0, v[164:165]
	global_load_lds_dwordx4 v[228:229], off
	v_lshl_add_u64 v[228:229], s[42:43], 0, v[164:165]
	s_add_i32 m0, s33, 0x2000
	s_nop 0
	global_load_lds_dwordx4 v[228:229], off
	v_lshl_add_u64 v[228:229], s[26:27], 0, v[162:163]
	s_mov_b32 m0, s34
	s_nop 0
	global_load_lds_dwordx4 v[228:229], off
	s_mov_b32 m0, s35
	s_nop 0
	global_load_lds_dwordx4 v[230:231], off
	s_waitcnt vmcnt(8) lgkmcnt(0)
	s_setprio 1
	s_barrier
	v_mfma_f32_16x16x32_bf16 v[62:65], v[102:105], v[166:169], v[62:65]
	v_mfma_f32_16x16x32_bf16 v[58:61], v[126:129], v[166:169], v[58:61]
	v_mfma_f32_16x16x32_bf16 v[46:49], v[102:105], v[200:203], v[46:49]
	v_mfma_f32_16x16x32_bf16 v[42:45], v[126:129], v[200:203], v[42:45]
	v_mfma_f32_16x16x32_bf16 v[30:33], v[102:105], v[208:211], v[30:33]
	v_mfma_f32_16x16x32_bf16 v[26:29], v[126:129], v[208:211], v[26:29]
	v_mfma_f32_16x16x32_bf16 v[14:17], v[102:105], v[216:219], v[14:17]
	v_mfma_f32_16x16x32_bf16 v[10:13], v[126:129], v[216:219], v[10:13]
	v_mfma_f32_16x16x32_bf16 v[62:65], v[114:117], v[176:179], v[62:65]
	v_mfma_f32_16x16x32_bf16 v[58:61], v[134:137], v[176:179], v[58:61]
	v_mfma_f32_16x16x32_bf16 v[46:49], v[114:117], v[204:207], v[46:49]
	v_mfma_f32_16x16x32_bf16 v[42:45], v[134:137], v[204:207], v[42:45]
	v_mfma_f32_16x16x32_bf16 v[30:33], v[114:117], v[212:215], v[30:33]
	v_mfma_f32_16x16x32_bf16 v[26:29], v[134:137], v[212:215], v[26:29]
	v_mfma_f32_16x16x32_bf16 v[14:17], v[114:117], v[220:223], v[14:17]
	v_mfma_f32_16x16x32_bf16 v[10:13], v[134:137], v[220:223], v[10:13]
	s_setprio 0
	s_setprio 1
	v_mfma_f32_16x16x32_bf16 v[54:57], v[138:141], v[166:169], v[54:57]
	v_mfma_f32_16x16x32_bf16 v[50:53], v[154:157], v[166:169], v[50:53]
	v_mfma_f32_16x16x32_bf16 v[38:41], v[138:141], v[200:203], v[38:41]
	v_mfma_f32_16x16x32_bf16 v[34:37], v[154:157], v[200:203], v[34:37]
	v_mfma_f32_16x16x32_bf16 v[22:25], v[138:141], v[208:211], v[22:25]
	v_mfma_f32_16x16x32_bf16 v[18:21], v[154:157], v[208:211], v[18:21]
	v_mfma_f32_16x16x32_bf16 v[6:9], v[138:141], v[216:219], v[6:9]
	v_mfma_f32_16x16x32_bf16 v[2:5], v[154:157], v[216:219], v[2:5]
	v_mfma_f32_16x16x32_bf16 v[54:57], v[146:149], v[176:179], v[54:57]
	v_mfma_f32_16x16x32_bf16 v[50:53], v[158:161], v[176:179], v[50:53]
	v_mfma_f32_16x16x32_bf16 v[38:41], v[146:149], v[204:207], v[38:41]
	v_mfma_f32_16x16x32_bf16 v[34:37], v[158:161], v[204:207], v[34:37]
	v_mfma_f32_16x16x32_bf16 v[22:25], v[146:149], v[212:215], v[22:25]
	v_mfma_f32_16x16x32_bf16 v[18:21], v[158:161], v[212:215], v[18:21]
	v_mfma_f32_16x16x32_bf16 v[6:9], v[146:149], v[220:223], v[6:9]
	v_mfma_f32_16x16x32_bf16 v[2:5], v[158:161], v[220:223], v[2:5]
	s_barrier
	s_setprio 0
	s_add_i32 s33, 0, 0x18000
	s_add_i32 s41, 0, 0x1c000
	v_add_u32_e32 v134, s33, v172
	v_add_u32_e32 v158, s41, v172
	ds_read_b128 v[102:105], v134
	ds_read_b128 v[114:117], v134 offset:1024
	ds_read_b128 v[126:129], v134 offset:2048
	ds_read_b128 v[134:137], v134 offset:3072
	ds_read_b128 v[138:141], v158
	ds_read_b128 v[146:149], v158 offset:1024
	ds_read_b128 v[154:157], v158 offset:2048
	ds_read_b128 v[158:161], v158 offset:3072
	ds_read_b128 v[166:169], v173 offset:32768
	ds_read_b128 v[176:179], v173 offset:33792
	ds_read_b128 v[200:203], v173 offset:34816
	ds_read_b128 v[204:207], v173 offset:35840
	ds_read_b128 v[208:211], v173 offset:36864
	ds_read_b128 v[212:215], v173 offset:37888
	ds_read_b128 v[216:219], v173 offset:38912
	ds_read_b128 v[220:223], v173 offset:39936
	s_add_u32 s26, s26, 0x10000
	s_addc_u32 s27, s27, 0
	s_mov_b32 m0, s36
	v_lshl_add_u64 v[232:233], s[26:27], 0, v[162:163]
	global_load_lds_dwordx4 v[232:233], off
	v_lshl_add_u64 v[232:233], s[26:27], 0, v[164:165]
	s_mov_b32 m0, s37
	s_nop 0
	global_load_lds_dwordx4 v[232:233], off
	s_waitcnt vmcnt(8) lgkmcnt(0)
	s_setprio 1
	s_barrier
	v_mfma_f32_16x16x32_bf16 v[150:153], v[102:105], v[166:169], v[150:153]
	v_mfma_f32_16x16x32_bf16 v[142:145], v[126:129], v[166:169], v[142:145]
	v_mfma_f32_16x16x32_bf16 v[118:121], v[102:105], v[200:203], v[118:121]
	v_mfma_f32_16x16x32_bf16 v[110:113], v[126:129], v[200:203], v[110:113]
	v_mfma_f32_16x16x32_bf16 v[94:97], v[102:105], v[208:211], v[94:97]
	v_mfma_f32_16x16x32_bf16 v[90:93], v[126:129], v[208:211], v[90:93]
	v_mfma_f32_16x16x32_bf16 v[78:81], v[102:105], v[216:219], v[78:81]
	v_mfma_f32_16x16x32_bf16 v[74:77], v[126:129], v[216:219], v[74:77]
	v_mfma_f32_16x16x32_bf16 v[150:153], v[114:117], v[176:179], v[150:153]
	v_mfma_f32_16x16x32_bf16 v[142:145], v[134:137], v[176:179], v[142:145]
	v_mfma_f32_16x16x32_bf16 v[118:121], v[114:117], v[204:207], v[118:121]
	v_mfma_f32_16x16x32_bf16 v[110:113], v[134:137], v[204:207], v[110:113]
	v_mfma_f32_16x16x32_bf16 v[94:97], v[114:117], v[212:215], v[94:97]
	v_mfma_f32_16x16x32_bf16 v[90:93], v[134:137], v[212:215], v[90:93]
	v_mfma_f32_16x16x32_bf16 v[78:81], v[114:117], v[220:223], v[78:81]
	v_mfma_f32_16x16x32_bf16 v[74:77], v[134:137], v[220:223], v[74:77]
	s_setprio 0
	s_setprio 1
	v_mfma_f32_16x16x32_bf16 v[130:133], v[138:141], v[166:169], v[130:133]
	v_mfma_f32_16x16x32_bf16 v[122:125], v[154:157], v[166:169], v[122:125]
	v_mfma_f32_16x16x32_bf16 v[106:109], v[138:141], v[200:203], v[106:109]
	v_mfma_f32_16x16x32_bf16 v[98:101], v[154:157], v[200:203], v[98:101]
	v_mfma_f32_16x16x32_bf16 v[86:89], v[138:141], v[208:211], v[86:89]
	v_mfma_f32_16x16x32_bf16 v[82:85], v[154:157], v[208:211], v[82:85]
	v_mfma_f32_16x16x32_bf16 v[70:73], v[138:141], v[216:219], v[70:73]
	v_mfma_f32_16x16x32_bf16 v[66:69], v[154:157], v[216:219], v[66:69]
	v_mfma_f32_16x16x32_bf16 v[130:133], v[146:149], v[176:179], v[130:133]
	v_mfma_f32_16x16x32_bf16 v[122:125], v[158:161], v[176:179], v[122:125]
	v_mfma_f32_16x16x32_bf16 v[106:109], v[146:149], v[204:207], v[106:109]
	v_mfma_f32_16x16x32_bf16 v[98:101], v[158:161], v[204:207], v[98:101]
	v_mfma_f32_16x16x32_bf16 v[86:89], v[146:149], v[212:215], v[86:89]
	v_mfma_f32_16x16x32_bf16 v[82:85], v[158:161], v[212:215], v[82:85]
	v_mfma_f32_16x16x32_bf16 v[70:73], v[146:149], v[220:223], v[70:73]
	v_mfma_f32_16x16x32_bf16 v[66:69], v[158:161], v[220:223], v[66:69]
	s_barrier
	s_setprio 0
	ds_read_b128 v[166:169], v173 offset:49152
	ds_read_b128 v[176:179], v173 offset:50176
	ds_read_b128 v[200:203], v173 offset:51200
	ds_read_b128 v[204:207], v173 offset:52224
	ds_read_b128 v[208:211], v173 offset:53248
	ds_read_b128 v[212:215], v173 offset:54272
	ds_read_b128 v[216:219], v173 offset:55296
	ds_read_b128 v[220:223], v173 offset:56320
	s_add_i32 s26, s33, s31
	v_lshl_add_u64 v[224:225], v[224:225], 0, s[90:91]
	s_mov_b32 m0, s26
	s_nop 0
	global_load_lds_dwordx4 v[224:225], off
	s_add_i32 m0, s26, 0x2000
	s_add_u32 s24, s24, 0x10080
	v_lshl_add_u64 v[224:225], v[226:227], 0, s[90:91]
	s_addc_u32 s25, s25, 0
	s_add_i32 s26, s41, s31
	global_load_lds_dwordx4 v[224:225], off
	v_lshl_add_u64 v[224:225], s[24:25], 0, v[162:163]
	s_mov_b32 m0, s26
	s_nop 0
	global_load_lds_dwordx4 v[224:225], off
	v_lshl_add_u64 v[224:225], s[24:25], 0, v[164:165]
	s_add_i32 m0, s26, 0x2000
	s_nop 0
	global_load_lds_dwordx4 v[224:225], off
	v_lshl_add_u64 v[224:225], v[228:229], 0, s[90:91]
	s_mov_b32 m0, s38
	s_nop 0
	global_load_lds_dwordx4 v[224:225], off
	v_lshl_add_u64 v[224:225], v[230:231], 0, s[90:91]
	s_mov_b32 m0, s39
	s_nop 0
	global_load_lds_dwordx4 v[224:225], off
	s_waitcnt vmcnt(8) lgkmcnt(0)
	s_setprio 1
	s_barrier
	v_mfma_f32_16x16x32_bf16 v[62:65], v[102:105], v[166:169], v[62:65]
	v_mfma_f32_16x16x32_bf16 v[58:61], v[126:129], v[166:169], v[58:61]
	v_mfma_f32_16x16x32_bf16 v[46:49], v[102:105], v[200:203], v[46:49]
	v_mfma_f32_16x16x32_bf16 v[42:45], v[126:129], v[200:203], v[42:45]
	v_mfma_f32_16x16x32_bf16 v[30:33], v[102:105], v[208:211], v[30:33]
	v_mfma_f32_16x16x32_bf16 v[26:29], v[126:129], v[208:211], v[26:29]
	v_mfma_f32_16x16x32_bf16 v[14:17], v[102:105], v[216:219], v[14:17]
	v_mfma_f32_16x16x32_bf16 v[10:13], v[126:129], v[216:219], v[10:13]
	v_mfma_f32_16x16x32_bf16 v[62:65], v[114:117], v[176:179], v[62:65]
	v_mfma_f32_16x16x32_bf16 v[58:61], v[134:137], v[176:179], v[58:61]
	v_mfma_f32_16x16x32_bf16 v[46:49], v[114:117], v[204:207], v[46:49]
	v_mfma_f32_16x16x32_bf16 v[42:45], v[134:137], v[204:207], v[42:45]
	v_mfma_f32_16x16x32_bf16 v[30:33], v[114:117], v[212:215], v[30:33]
	v_mfma_f32_16x16x32_bf16 v[26:29], v[134:137], v[212:215], v[26:29]
	v_mfma_f32_16x16x32_bf16 v[14:17], v[114:117], v[220:223], v[14:17]
	v_mfma_f32_16x16x32_bf16 v[10:13], v[134:137], v[220:223], v[10:13]
	s_setprio 0
	s_setprio 1
	v_mfma_f32_16x16x32_bf16 v[54:57], v[138:141], v[166:169], v[54:57]
	v_mfma_f32_16x16x32_bf16 v[50:53], v[154:157], v[166:169], v[50:53]
	v_mfma_f32_16x16x32_bf16 v[38:41], v[138:141], v[200:203], v[38:41]
	v_mfma_f32_16x16x32_bf16 v[34:37], v[154:157], v[200:203], v[34:37]
	v_mfma_f32_16x16x32_bf16 v[22:25], v[138:141], v[208:211], v[22:25]
	v_mfma_f32_16x16x32_bf16 v[18:21], v[154:157], v[208:211], v[18:21]
	v_mfma_f32_16x16x32_bf16 v[6:9], v[138:141], v[216:219], v[6:9]
	v_mfma_f32_16x16x32_bf16 v[2:5], v[154:157], v[216:219], v[2:5]
	v_mfma_f32_16x16x32_bf16 v[54:57], v[146:149], v[176:179], v[54:57]
	v_mfma_f32_16x16x32_bf16 v[50:53], v[158:161], v[176:179], v[50:53]
	v_mfma_f32_16x16x32_bf16 v[38:41], v[146:149], v[204:207], v[38:41]
	v_mfma_f32_16x16x32_bf16 v[34:37], v[158:161], v[204:207], v[34:37]
	v_mfma_f32_16x16x32_bf16 v[22:25], v[146:149], v[212:215], v[22:25]
	v_mfma_f32_16x16x32_bf16 v[18:21], v[158:161], v[212:215], v[18:21]
	v_mfma_f32_16x16x32_bf16 v[6:9], v[146:149], v[220:223], v[6:9]
	v_mfma_f32_16x16x32_bf16 v[2:5], v[158:161], v[220:223], v[2:5]
	s_barrier
	s_setprio 0
	s_and_b64 vcc, exec, s[22:23]
	s_mov_b64 s[24:25], -1
	s_mov_b64 s[22:23], 0
	s_movk_i32 s26, 0x100
	s_cbranch_vccnz .LBB0_843
	s_andn2_b64 vcc, exec, s[10:11]
	s_cbranch_vccnz .LBB0_846
	s_barrier

.LBB0_996:
	s_add_i32 s45, 0, 0x10000
	s_add_i32 s48, 0, 0x14000
	v_add_u32_e32 v142, s45, v171
	v_add_u32_e32 v168, s48, v171
	ds_read_b128 v[130:133], v142
	ds_read_b128 v[134:137], v142 offset:1024
	ds_read_b128 v[138:141], v142 offset:2048
	ds_read_b128 v[142:145], v142 offset:3072
	ds_read_b128 v[146:149], v168
	ds_read_b128 v[158:161], v168 offset:1024
	ds_read_b128 v[164:167], v168 offset:2048
	ds_read_b128 v[174:177], v168 offset:3072
	ds_read_b128 v[200:203], v172
	ds_read_b128 v[204:207], v172 offset:1024
	ds_read_b128 v[208:211], v172 offset:2048
	ds_read_b128 v[212:215], v172 offset:3072
	ds_read_b128 v[216:219], v172 offset:4096
	ds_read_b128 v[220:223], v172 offset:5120
	ds_read_b128 v[224:227], v172 offset:6144
	ds_read_b128 v[228:231], v172 offset:7168
	s_add_u32 s22, s20, 0xfffc0080
	s_addc_u32 s23, s21, -1
	s_cmp_eq_u32 s44, 12
	s_cselect_b32 s25, s9, s23
	s_cselect_b32 s24, s40, s22
	s_cselect_b32 s23, s11, s43
	s_cselect_b32 s22, s41, s42
	v_lshl_add_u64 v[168:169], s[20:21], 0, v[156:157]
	s_add_i32 m0, s33, 0xc000
	s_nop 0
	global_load_lds_dwordx4 v[168:169], off
	v_lshl_add_u64 v[168:169], s[20:21], 0, v[154:155]
	s_add_i32 m0, s33, 0xe000
	s_nop 0
	global_load_lds_dwordx4 v[168:169], off
	s_waitcnt vmcnt(8) lgkmcnt(0)
	s_setprio 1
	s_barrier
	v_mfma_f32_16x16x32_bf16 v[126:129], v[130:133], v[200:203], v[126:129]
	v_mfma_f32_16x16x32_bf16 v[122:125], v[138:141], v[200:203], v[122:125]
	v_mfma_f32_16x16x32_bf16 v[110:113], v[130:133], v[208:211], v[110:113]
	v_mfma_f32_16x16x32_bf16 v[106:109], v[138:141], v[208:211], v[106:109]
	v_mfma_f32_16x16x32_bf16 v[98:101], v[130:133], v[216:219], v[98:101]
	v_mfma_f32_16x16x32_bf16 v[90:93], v[138:141], v[216:219], v[90:93]
	v_mfma_f32_16x16x32_bf16 v[86:89], v[130:133], v[224:227], v[86:89]
	v_mfma_f32_16x16x32_bf16 v[78:81], v[138:141], v[224:227], v[78:81]
	v_mfma_f32_16x16x32_bf16 v[126:129], v[134:137], v[204:207], v[126:129]
	v_mfma_f32_16x16x32_bf16 v[122:125], v[142:145], v[204:207], v[122:125]
	v_mfma_f32_16x16x32_bf16 v[110:113], v[134:137], v[212:215], v[110:113]
	v_mfma_f32_16x16x32_bf16 v[106:109], v[142:145], v[212:215], v[106:109]
	v_mfma_f32_16x16x32_bf16 v[98:101], v[134:137], v[220:223], v[98:101]
	v_mfma_f32_16x16x32_bf16 v[90:93], v[142:145], v[220:223], v[90:93]
	v_mfma_f32_16x16x32_bf16 v[86:89], v[134:137], v[228:231], v[86:89]
	v_mfma_f32_16x16x32_bf16 v[78:81], v[142:145], v[228:231], v[78:81]
	s_setprio 0
	s_setprio 1
	v_mfma_f32_16x16x32_bf16 v[118:121], v[146:149], v[200:203], v[118:121]
	v_mfma_f32_16x16x32_bf16 v[114:117], v[164:167], v[200:203], v[114:117]
	v_mfma_f32_16x16x32_bf16 v[102:105], v[146:149], v[208:211], v[102:105]
	v_mfma_f32_16x16x32_bf16 v[94:97], v[164:167], v[208:211], v[94:97]
	v_mfma_f32_16x16x32_bf16 v[82:85], v[146:149], v[216:219], v[82:85]
	v_mfma_f32_16x16x32_bf16 v[74:77], v[164:167], v[216:219], v[74:77]
	v_mfma_f32_16x16x32_bf16 v[70:73], v[146:149], v[224:227], v[70:73]
	v_mfma_f32_16x16x32_bf16 v[66:69], v[164:167], v[224:227], v[66:69]
	v_mfma_f32_16x16x32_bf16 v[118:121], v[158:161], v[204:207], v[118:121]
	v_mfma_f32_16x16x32_bf16 v[114:117], v[174:177], v[204:207], v[114:117]
	v_mfma_f32_16x16x32_bf16 v[102:105], v[158:161], v[212:215], v[102:105]
	v_mfma_f32_16x16x32_bf16 v[94:97], v[174:177], v[212:215], v[94:97]
	v_mfma_f32_16x16x32_bf16 v[82:85], v[158:161], v[220:223], v[82:85]
	v_mfma_f32_16x16x32_bf16 v[74:77], v[174:177], v[220:223], v[74:77]
	v_mfma_f32_16x16x32_bf16 v[70:73], v[158:161], v[228:231], v[70:73]
	v_mfma_f32_16x16x32_bf16 v[66:69], v[174:177], v[228:231], v[66:69]
	s_barrier
	s_setprio 0
	ds_read_b128 v[200:203], v172 offset:16384
	ds_read_b128 v[204:207], v172 offset:17408
	ds_read_b128 v[208:211], v172 offset:18432
	ds_read_b128 v[212:215], v172 offset:19456
	ds_read_b128 v[216:219], v172 offset:20480
	ds_read_b128 v[220:223], v172 offset:21504
	ds_read_b128 v[224:227], v172 offset:22528
	ds_read_b128 v[228:231], v172 offset:23552
	s_add_i32 s45, s45, s31
	v_lshl_add_u64 v[168:169], s[22:23], 0, v[162:163]
	s_mov_b32 m0, s45
	s_nop 0
	global_load_lds_dwordx4 v[168:169], off
	s_add_i32 m0, s45, 0x2000
	s_add_u32 s46, s22, 0x40000
	v_lshl_add_u64 v[178:179], s[22:23], 0, v[150:151]
	s_addc_u32 s47, s23, 0
	s_add_i32 s45, s48, s31
	global_load_lds_dwordx4 v[178:179], off
	v_lshl_add_u64 v[232:233], s[46:47], 0, v[162:163]
	s_mov_b32 m0, s45
	v_lshl_add_u64 v[234:235], s[24:25], 0, v[150:151]
	global_load_lds_dwordx4 v[232:233], off
	v_lshl_add_u64 v[232:233], s[46:47], 0, v[150:151]
	s_add_i32 m0, s45, 0x2000
	s_nop 0
	global_load_lds_dwordx4 v[232:233], off
	v_lshl_add_u64 v[232:233], s[24:25], 0, v[162:163]
	s_mov_b32 m0, s33
	s_nop 0
	global_load_lds_dwordx4 v[232:233], off
	s_mov_b32 m0, s34
	s_nop 0
	global_load_lds_dwordx4 v[234:235], off
	s_waitcnt vmcnt(8) lgkmcnt(0)
	s_setprio 1
	s_barrier
	v_mfma_f32_16x16x32_bf16 v[62:65], v[130:133], v[200:203], v[62:65]
	v_mfma_f32_16x16x32_bf16 v[58:61], v[138:141], v[200:203], v[58:61]
	v_mfma_f32_16x16x32_bf16 v[50:53], v[130:133], v[208:211], v[50:53]
	v_mfma_f32_16x16x32_bf16 v[42:45], v[138:141], v[208:211], v[42:45]
	v_mfma_f32_16x16x32_bf16 v[34:37], v[130:133], v[216:219], v[34:37]
	v_mfma_f32_16x16x32_bf16 v[26:29], v[138:141], v[216:219], v[26:29]
	v_mfma_f32_16x16x32_bf16 v[18:21], v[130:133], v[224:227], v[18:21]
	v_mfma_f32_16x16x32_bf16 v[10:13], v[138:141], v[224:227], v[10:13]
	v_mfma_f32_16x16x32_bf16 v[62:65], v[134:137], v[204:207], v[62:65]
	v_mfma_f32_16x16x32_bf16 v[58:61], v[142:145], v[204:207], v[58:61]
	v_mfma_f32_16x16x32_bf16 v[50:53], v[134:137], v[212:215], v[50:53]
	v_mfma_f32_16x16x32_bf16 v[42:45], v[142:145], v[212:215], v[42:45]
	v_mfma_f32_16x16x32_bf16 v[34:37], v[134:137], v[220:223], v[34:37]
	v_mfma_f32_16x16x32_bf16 v[26:29], v[142:145], v[220:223], v[26:29]
	v_mfma_f32_16x16x32_bf16 v[18:21], v[134:137], v[228:231], v[18:21]
	v_mfma_f32_16x16x32_bf16 v[10:13], v[142:145], v[228:231], v[10:13]
	s_setprio 0
	s_setprio 1
	v_mfma_f32_16x16x32_bf16 v[54:57], v[146:149], v[200:203], v[54:57]
	v_mfma_f32_16x16x32_bf16 v[46:49], v[164:167], v[200:203], v[46:49]
	v_mfma_f32_16x16x32_bf16 v[38:41], v[146:149], v[208:211], v[38:41]
	v_mfma_f32_16x16x32_bf16 v[30:33], v[164:167], v[208:211], v[30:33]
	v_mfma_f32_16x16x32_bf16 v[22:25], v[146:149], v[216:219], v[22:25]
	v_mfma_f32_16x16x32_bf16 v[14:17], v[164:167], v[216:219], v[14:17]
	v_mfma_f32_16x16x32_bf16 v[6:9], v[146:149], v[224:227], v[6:9]
	v_mfma_f32_16x16x32_bf16 v[2:5], v[164:167], v[224:227], v[2:5]
	v_mfma_f32_16x16x32_bf16 v[54:57], v[158:161], v[204:207], v[54:57]
	v_mfma_f32_16x16x32_bf16 v[46:49], v[174:177], v[204:207], v[46:49]
	v_mfma_f32_16x16x32_bf16 v[38:41], v[158:161], v[212:215], v[38:41]
	v_mfma_f32_16x16x32_bf16 v[30:33], v[174:177], v[212:215], v[30:33]
	v_mfma_f32_16x16x32_bf16 v[22:25], v[158:161], v[220:223], v[22:25]
	v_mfma_f32_16x16x32_bf16 v[14:17], v[174:177], v[220:223], v[14:17]
	v_mfma_f32_16x16x32_bf16 v[6:9], v[158:161], v[228:231], v[6:9]
	v_mfma_f32_16x16x32_bf16 v[2:5], v[174:177], v[228:231], v[2:5]
	s_barrier
	s_setprio 0
	s_add_i32 s45, 0, 0x18000
	s_add_i32 s46, 0, 0x1c000
	v_add_u32_e32 v142, s45, v171
	v_add_u32_e32 v173, s46, v171
	ds_read_b128 v[130:133], v142
	ds_read_b128 v[134:137], v142 offset:1024
	ds_read_b128 v[138:141], v142 offset:2048
	ds_read_b128 v[142:145], v142 offset:3072
	ds_read_b128 v[146:149], v173
	ds_read_b128 v[158:161], v173 offset:1024
	ds_read_b128 v[164:167], v173 offset:2048
	ds_read_b128 v[174:177], v173 offset:3072
	ds_read_b128 v[200:203], v172 offset:32768
	ds_read_b128 v[204:207], v172 offset:33792
	ds_read_b128 v[208:211], v172 offset:34816
	ds_read_b128 v[212:215], v172 offset:35840
	ds_read_b128 v[216:219], v172 offset:36864
	ds_read_b128 v[220:223], v172 offset:37888
	ds_read_b128 v[224:227], v172 offset:38912
	ds_read_b128 v[228:231], v172 offset:39936
	s_add_u32 s24, s24, 0x40000
	s_addc_u32 s25, s25, 0
	s_mov_b32 m0, s35
	v_lshl_add_u64 v[236:237], s[24:25], 0, v[162:163]
	global_load_lds_dwordx4 v[236:237], off
	v_lshl_add_u64 v[236:237], s[24:25], 0, v[150:151]
	s_mov_b32 m0, s36
	s_nop 0
	global_load_lds_dwordx4 v[236:237], off
	s_waitcnt vmcnt(8) lgkmcnt(0)
	s_setprio 1
	s_barrier
	v_mfma_f32_16x16x32_bf16 v[126:129], v[130:133], v[200:203], v[126:129]
	v_mfma_f32_16x16x32_bf16 v[122:125], v[138:141], v[200:203], v[122:125]
	v_mfma_f32_16x16x32_bf16 v[110:113], v[130:133], v[208:211], v[110:113]
	v_mfma_f32_16x16x32_bf16 v[106:109], v[138:141], v[208:211], v[106:109]
	v_mfma_f32_16x16x32_bf16 v[98:101], v[130:133], v[216:219], v[98:101]
	v_mfma_f32_16x16x32_bf16 v[90:93], v[138:141], v[216:219], v[90:93]
	v_mfma_f32_16x16x32_bf16 v[86:89], v[130:133], v[224:227], v[86:89]
	v_mfma_f32_16x16x32_bf16 v[78:81], v[138:141], v[224:227], v[78:81]
	v_mfma_f32_16x16x32_bf16 v[126:129], v[134:137], v[204:207], v[126:129]
	v_mfma_f32_16x16x32_bf16 v[122:125], v[142:145], v[204:207], v[122:125]
	v_mfma_f32_16x16x32_bf16 v[110:113], v[134:137], v[212:215], v[110:113]
	v_mfma_f32_16x16x32_bf16 v[106:109], v[142:145], v[212:215], v[106:109]
	v_mfma_f32_16x16x32_bf16 v[98:101], v[134:137], v[220:223], v[98:101]
	v_mfma_f32_16x16x32_bf16 v[90:93], v[142:145], v[220:223], v[90:93]
	v_mfma_f32_16x16x32_bf16 v[86:89], v[134:137], v[228:231], v[86:89]
	v_mfma_f32_16x16x32_bf16 v[78:81], v[142:145], v[228:231], v[78:81]
	s_setprio 0
	s_setprio 1
	v_mfma_f32_16x16x32_bf16 v[118:121], v[146:149], v[200:203], v[118:121]
	v_mfma_f32_16x16x32_bf16 v[114:117], v[164:167], v[200:203], v[114:117]
	v_mfma_f32_16x16x32_bf16 v[102:105], v[146:149], v[208:211], v[102:105]
	v_mfma_f32_16x16x32_bf16 v[94:97], v[164:167], v[208:211], v[94:97]
	v_mfma_f32_16x16x32_bf16 v[82:85], v[146:149], v[216:219], v[82:85]
	v_mfma_f32_16x16x32_bf16 v[74:77], v[164:167], v[216:219], v[74:77]
	v_mfma_f32_16x16x32_bf16 v[70:73], v[146:149], v[224:227], v[70:73]
	v_mfma_f32_16x16x32_bf16 v[66:69], v[164:167], v[224:227], v[66:69]
	v_mfma_f32_16x16x32_bf16 v[118:121], v[158:161], v[204:207], v[118:121]
	v_mfma_f32_16x16x32_bf16 v[114:117], v[174:177], v[204:207], v[114:117]
	v_mfma_f32_16x16x32_bf16 v[102:105], v[158:161], v[212:215], v[102:105]
	v_mfma_f32_16x16x32_bf16 v[94:97], v[174:177], v[212:215], v[94:97]
	v_mfma_f32_16x16x32_bf16 v[82:85], v[158:161], v[220:223], v[82:85]
	v_mfma_f32_16x16x32_bf16 v[74:77], v[174:177], v[220:223], v[74:77]
	v_mfma_f32_16x16x32_bf16 v[70:73], v[158:161], v[228:231], v[70:73]
	v_mfma_f32_16x16x32_bf16 v[66:69], v[174:177], v[228:231], v[66:69]
	s_barrier
	s_setprio 0
	ds_read_b128 v[200:203], v172 offset:49152
	ds_read_b128 v[204:207], v172 offset:50176
	ds_read_b128 v[208:211], v172 offset:51200
	ds_read_b128 v[212:215], v172 offset:52224
	ds_read_b128 v[216:219], v172 offset:53248
	ds_read_b128 v[220:223], v172 offset:54272
	ds_read_b128 v[224:227], v172 offset:55296
	ds_read_b128 v[228:231], v172 offset:56320
	s_add_i32 s24, s45, s31
	v_lshl_add_u64 v[168:169], v[168:169], 0, s[90:91]
	s_mov_b32 m0, s24
	s_nop 0
	global_load_lds_dwordx4 v[168:169], off
	s_add_i32 m0, s24, 0x2000
	s_add_u32 s22, s22, 0x40080
	v_lshl_add_u64 v[168:169], v[178:179], 0, s[90:91]
	s_addc_u32 s23, s23, 0
	s_add_i32 s24, s46, s31
	global_load_lds_dwordx4 v[168:169], off
	v_lshl_add_u64 v[168:169], s[22:23], 0, v[162:163]
	s_mov_b32 m0, s24
	s_nop 0
	global_load_lds_dwordx4 v[168:169], off
	v_lshl_add_u64 v[168:169], s[22:23], 0, v[150:151]
	s_add_i32 m0, s24, 0x2000
	s_nop 0
	global_load_lds_dwordx4 v[168:169], off
	v_lshl_add_u64 v[168:169], v[232:233], 0, s[90:91]
	s_mov_b32 m0, s37
	s_nop 0
	global_load_lds_dwordx4 v[168:169], off
	v_lshl_add_u64 v[168:169], v[234:235], 0, s[90:91]
	s_mov_b32 m0, s38
	s_nop 0
	global_load_lds_dwordx4 v[168:169], off
	s_waitcnt vmcnt(8) lgkmcnt(0)
	s_setprio 1
	s_barrier
	v_mfma_f32_16x16x32_bf16 v[62:65], v[130:133], v[200:203], v[62:65]
	v_mfma_f32_16x16x32_bf16 v[58:61], v[138:141], v[200:203], v[58:61]
	v_mfma_f32_16x16x32_bf16 v[50:53], v[130:133], v[208:211], v[50:53]
	v_mfma_f32_16x16x32_bf16 v[42:45], v[138:141], v[208:211], v[42:45]
	v_mfma_f32_16x16x32_bf16 v[34:37], v[130:133], v[216:219], v[34:37]
	v_mfma_f32_16x16x32_bf16 v[26:29], v[138:141], v[216:219], v[26:29]
	v_mfma_f32_16x16x32_bf16 v[18:21], v[130:133], v[224:227], v[18:21]
	v_mfma_f32_16x16x32_bf16 v[10:13], v[138:141], v[224:227], v[10:13]
	v_mfma_f32_16x16x32_bf16 v[62:65], v[134:137], v[204:207], v[62:65]
	v_mfma_f32_16x16x32_bf16 v[58:61], v[142:145], v[204:207], v[58:61]
	v_mfma_f32_16x16x32_bf16 v[50:53], v[134:137], v[212:215], v[50:53]
	v_mfma_f32_16x16x32_bf16 v[42:45], v[142:145], v[212:215], v[42:45]
	v_mfma_f32_16x16x32_bf16 v[34:37], v[134:137], v[220:223], v[34:37]
	v_mfma_f32_16x16x32_bf16 v[26:29], v[142:145], v[220:223], v[26:29]
	v_mfma_f32_16x16x32_bf16 v[18:21], v[134:137], v[228:231], v[18:21]
	v_mfma_f32_16x16x32_bf16 v[10:13], v[142:145], v[228:231], v[10:13]
	s_setprio 0
	s_setprio 1
	v_mfma_f32_16x16x32_bf16 v[54:57], v[146:149], v[200:203], v[54:57]
	v_mfma_f32_16x16x32_bf16 v[46:49], v[164:167], v[200:203], v[46:49]
	v_mfma_f32_16x16x32_bf16 v[38:41], v[146:149], v[208:211], v[38:41]
	v_mfma_f32_16x16x32_bf16 v[30:33], v[164:167], v[208:211], v[30:33]
	v_mfma_f32_16x16x32_bf16 v[22:25], v[146:149], v[216:219], v[22:25]
	v_mfma_f32_16x16x32_bf16 v[14:17], v[164:167], v[216:219], v[14:17]
	v_mfma_f32_16x16x32_bf16 v[6:9], v[146:149], v[224:227], v[6:9]
	v_mfma_f32_16x16x32_bf16 v[2:5], v[164:167], v[224:227], v[2:5]
	v_mfma_f32_16x16x32_bf16 v[54:57], v[158:161], v[204:207], v[54:57]
	v_mfma_f32_16x16x32_bf16 v[46:49], v[174:177], v[204:207], v[46:49]
	v_mfma_f32_16x16x32_bf16 v[38:41], v[158:161], v[212:215], v[38:41]
	v_mfma_f32_16x16x32_bf16 v[30:33], v[174:177], v[212:215], v[30:33]
	v_mfma_f32_16x16x32_bf16 v[22:25], v[158:161], v[220:223], v[22:25]
	v_mfma_f32_16x16x32_bf16 v[14:17], v[174:177], v[220:223], v[14:17]
	v_mfma_f32_16x16x32_bf16 v[6:9], v[158:161], v[228:231], v[6:9]
	v_mfma_f32_16x16x32_bf16 v[2:5], v[174:177], v[228:231], v[2:5]
	s_barrier
	s_setprio 0
	s_add_i32 s44, s44, 2
	s_add_u32 s42, s42, 0x100
	s_addc_u32 s43, s43, 0
	s_add_u32 s20, s20, 0x100
	s_addc_u32 s21, s21, 0
	s_cmp_lt_u32 s44, 14
	s_cbranch_scc1 .LBB0_996
	v_readlane_b32 s40, v254, 24
	s_andn2_b64 vcc, exec, s[6:7]
	v_readlane_b32 s42, v254, 26
	v_readlane_b32 s43, v254, 27
	v_readlane_b32 s44, v254, 28
	v_readlane_b32 s45, v254, 29
	v_readlane_b32 s46, v254, 30
	v_readlane_b32 s47, v254, 31
	v_readlane_b32 s50, v254, 34
	v_readlane_b32 s51, v254, 35
	v_readlane_b32 s41, v254, 25
	v_readlane_b32 s48, v254, 32
	v_readlane_b32 s49, v254, 33
	v_readlane_b32 s52, v254, 36
	v_readlane_b32 s53, v254, 37
	v_readlane_b32 s54, v254, 38
	v_readlane_b32 s55, v254, 39
	s_cbranch_vccnz .LBB0_999
	s_barrier

.LBB0_1303:
	ds_read_b128 v[2:5], v200
	ds_read_b128 v[6:9], v201
	ds_read_b128 v[10:13], v202
	ds_read_b128 v[14:17], v203
	ds_read_b128 v[18:21], v204
	ds_read_b128 v[22:25], v205
	ds_read_b128 v[26:29], v206
	ds_read_b128 v[30:33], v207
	s_lshl_b32 s21, s56, 10
	v_add_u32_e32 v217, s21, v177
	ds_read_b128 v[34:37], v216
	ds_read_b128 v[38:41], v216 offset:1024
	ds_read_b128 v[42:45], v216 offset:2048
	ds_read_b128 v[46:49], v216 offset:3072
	ds_read_b32 v66, v217 offset:512
	ds_read_b128 v[50:53], v216 offset:4096
	ds_read_b128 v[54:57], v216 offset:5120
	ds_read_b128 v[58:61], v216 offset:6144
	ds_read_b128 v[62:65], v216 offset:7168
	s_add_i32 s21, s36, 0xc000
	s_waitcnt lgkmcnt(0)
	v_lshl_add_u32 v66, v66, 10, v176
	s_mov_b32 m0, s21
	s_add_i32 s57, s36, 0xe000
	global_load_lds_dwordx4 v66, s[12:13]
	ds_read_b32 v66, v217 offset:768
	s_mov_b32 m0, s57
	s_waitcnt lgkmcnt(0)
	v_lshl_add_u32 v66, v66, 10, v176
	global_load_lds_dwordx4 v66, s[12:13]
	s_waitcnt vmcnt(8) lgkmcnt(0)
	s_setprio 1
	s_barrier
	v_mfma_f32_16x16x128_f8f6f4 v[154:157], v[2:9], v[34:41], 0
	v_mfma_f32_16x16x128_f8f6f4 v[146:149], v[10:17], v[34:41], 0
	v_mfma_f32_16x16x128_f8f6f4 v[138:141], v[2:9], v[42:49], 0
	v_mfma_f32_16x16x128_f8f6f4 v[130:133], v[10:17], v[42:49], 0
	v_mfma_f32_16x16x128_f8f6f4 v[122:125], v[2:9], v[50:57], 0
	v_mfma_f32_16x16x128_f8f6f4 v[114:117], v[10:17], v[50:57], 0
	v_mfma_f32_16x16x128_f8f6f4 v[106:109], v[2:9], v[58:65], 0
	v_mfma_f32_16x16x128_f8f6f4 v[98:101], v[10:17], v[58:65], 0
	s_setprio 0
	s_setprio 1
	v_mfma_f32_16x16x128_f8f6f4 v[158:161], v[18:25], v[34:41], 0
	v_mfma_f32_16x16x128_f8f6f4 v[150:153], v[26:33], v[34:41], 0
	v_mfma_f32_16x16x128_f8f6f4 v[142:145], v[18:25], v[42:49], 0
	v_mfma_f32_16x16x128_f8f6f4 v[134:137], v[26:33], v[42:49], 0
	v_mfma_f32_16x16x128_f8f6f4 v[126:129], v[18:25], v[50:57], 0
	v_mfma_f32_16x16x128_f8f6f4 v[118:121], v[26:33], v[50:57], 0
	v_mfma_f32_16x16x128_f8f6f4 v[110:113], v[18:25], v[58:65], 0
	v_mfma_f32_16x16x128_f8f6f4 v[102:105], v[26:33], v[58:65], 0
	s_barrier
	s_setprio 0
	v_lshl_add_u64 v[172:173], s[26:27], 0, v[164:165]
	s_mov_b64 s[28:29], 0x100
	s_mov_b32 m0, s37
	v_lshl_add_u64 v[34:35], v[172:173], 0, s[28:29]
	v_lshl_add_u64 v[174:175], s[26:27], 0, v[166:167]
	ds_read_b128 v[218:221], v216 offset:16384
	ds_read_b128 v[222:225], v216 offset:17408
	ds_read_b128 v[226:229], v216 offset:18432
	ds_read_b128 v[230:233], v216 offset:19456
	ds_read_b128 v[234:237], v216 offset:20480
	ds_read_b128 v[238:241], v216 offset:21504
	ds_read_b128 v[242:245], v216 offset:22528
	ds_read_b128 v[246:249], v216 offset:23552
	global_load_lds_dwordx4 v[34:35], off
	v_lshl_add_u64 v[34:35], v[174:175], 0, s[28:29]
	s_add_u32 s28, s26, 0x20100
	s_mov_b32 m0, s38
	s_addc_u32 s29, s27, 0
	global_load_lds_dwordx4 v[34:35], off
	v_lshl_add_u64 v[34:35], s[28:29], 0, v[164:165]
	s_mov_b32 m0, s39
	s_nop 0
	global_load_lds_dwordx4 v[34:35], off
	v_lshl_add_u64 v[34:35], s[28:29], 0, v[166:167]
	s_mov_b32 m0, s40
	s_nop 0
	global_load_lds_dwordx4 v[34:35], off
	ds_read_b32 v34, v217
	s_mov_b32 m0, s36
	s_waitcnt lgkmcnt(0)
	v_lshl_add_u32 v34, v34, 10, v176
	global_load_lds_dwordx4 v34, s[14:15]
	ds_read_b32 v34, v217 offset:256
	s_mov_b32 m0, s41
	s_waitcnt lgkmcnt(0)
	v_lshl_add_u32 v34, v34, 10, v176
	global_load_lds_dwordx4 v34, s[14:15]
	s_waitcnt vmcnt(8) lgkmcnt(0)
	s_setprio 1
	s_barrier
	v_mfma_f32_16x16x128_f8f6f4 v[90:93], v[2:9], v[218:225], 0
	v_mfma_f32_16x16x128_f8f6f4 v[82:85], v[10:17], v[218:225], 0
	v_mfma_f32_16x16x128_f8f6f4 v[74:77], v[2:9], v[226:233], 0
	v_mfma_f32_16x16x128_f8f6f4 v[66:69], v[10:17], v[226:233], 0
	v_mfma_f32_16x16x128_f8f6f4 v[58:61], v[2:9], v[234:241], 0
	v_mfma_f32_16x16x128_f8f6f4 v[50:53], v[10:17], v[234:241], 0
	v_mfma_f32_16x16x128_f8f6f4 v[42:45], v[2:9], v[242:249], 0
	v_mfma_f32_16x16x128_f8f6f4 v[34:37], v[10:17], v[242:249], 0
	s_setprio 0
	s_setprio 1
	v_mfma_f32_16x16x128_f8f6f4 v[94:97], v[18:25], v[218:225], 0
	v_mfma_f32_16x16x128_f8f6f4 v[86:89], v[26:33], v[218:225], 0
	v_mfma_f32_16x16x128_f8f6f4 v[78:81], v[18:25], v[226:233], 0
	v_mfma_f32_16x16x128_f8f6f4 v[70:73], v[26:33], v[226:233], 0
	v_mfma_f32_16x16x128_f8f6f4 v[62:65], v[18:25], v[234:241], 0
	v_mfma_f32_16x16x128_f8f6f4 v[54:57], v[26:33], v[234:241], 0
	v_mfma_f32_16x16x128_f8f6f4 v[46:49], v[18:25], v[242:249], 0
	v_mfma_f32_16x16x128_f8f6f4 v[38:41], v[26:33], v[242:249], 0
	s_barrier
	s_setprio 0
	ds_read_b128 v[18:21], v208
	ds_read_b128 v[22:25], v209
	ds_read_b128 v[26:29], v210
	ds_read_b128 v[30:33], v211
	ds_read_b128 v[2:5], v212
	ds_read_b128 v[6:9], v213
	ds_read_b128 v[10:13], v214
	ds_read_b128 v[14:17], v215
	ds_read_b128 v[218:221], v216 offset:32768
	ds_read_b128 v[222:225], v216 offset:33792
	ds_read_b128 v[226:229], v216 offset:34816
	ds_read_b128 v[230:233], v216 offset:35840
	ds_read_b32 v162, v217 offset:512
	ds_read_b128 v[234:237], v216 offset:36864
	ds_read_b128 v[238:241], v216 offset:37888
	ds_read_b128 v[242:245], v216 offset:38912
	ds_read_b128 v[246:249], v216 offset:39936
	s_waitcnt lgkmcnt(0)
	v_lshl_add_u32 v162, v162, 10, v176
	s_mov_b32 m0, s42
	s_nop 0
	global_load_lds_dwordx4 v162, s[14:15]
	ds_read_b32 v162, v217 offset:768
	s_mov_b32 m0, s43
	s_waitcnt lgkmcnt(0)
	v_lshl_add_u32 v162, v162, 10, v176
	global_load_lds_dwordx4 v162, s[14:15]
	s_waitcnt vmcnt(8) lgkmcnt(0)
	s_setprio 1
	s_barrier
	v_mfma_f32_16x16x128_f8f6f4 v[154:157], v[18:25], v[218:225], v[154:157]
	v_mfma_f32_16x16x128_f8f6f4 v[146:149], v[26:33], v[218:225], v[146:149]
	v_mfma_f32_16x16x128_f8f6f4 v[138:141], v[18:25], v[226:233], v[138:141]
	v_mfma_f32_16x16x128_f8f6f4 v[130:133], v[26:33], v[226:233], v[130:133]
	v_mfma_f32_16x16x128_f8f6f4 v[122:125], v[18:25], v[234:241], v[122:125]
	v_mfma_f32_16x16x128_f8f6f4 v[114:117], v[26:33], v[234:241], v[114:117]
	v_mfma_f32_16x16x128_f8f6f4 v[106:109], v[18:25], v[242:249], v[106:109]
	v_mfma_f32_16x16x128_f8f6f4 v[98:101], v[26:33], v[242:249], v[98:101]
	s_setprio 0
	s_setprio 1
	v_mfma_f32_16x16x128_f8f6f4 v[158:161], v[2:9], v[218:225], v[158:161]
	v_mfma_f32_16x16x128_f8f6f4 v[150:153], v[10:17], v[218:225], v[150:153]
	v_mfma_f32_16x16x128_f8f6f4 v[142:145], v[2:9], v[226:233], v[142:145]
	v_mfma_f32_16x16x128_f8f6f4 v[134:137], v[10:17], v[226:233], v[134:137]
	v_mfma_f32_16x16x128_f8f6f4 v[126:129], v[2:9], v[234:241], v[126:129]
	v_mfma_f32_16x16x128_f8f6f4 v[118:121], v[10:17], v[234:241], v[118:121]
	v_mfma_f32_16x16x128_f8f6f4 v[110:113], v[2:9], v[242:249], v[110:113]
	v_mfma_f32_16x16x128_f8f6f4 v[102:105], v[10:17], v[242:249], v[102:105]
	s_barrier
	s_setprio 0
	s_mov_b64 s[28:29], 0x180
	s_mov_b32 m0, s44
	v_lshl_add_u64 v[172:173], v[172:173], 0, s[28:29]
	ds_read_b128 v[218:221], v216 offset:49152
	ds_read_b128 v[222:225], v216 offset:50176
	ds_read_b128 v[226:229], v216 offset:51200
	ds_read_b128 v[230:233], v216 offset:52224
	ds_read_b128 v[234:237], v216 offset:53248
	ds_read_b128 v[238:241], v216 offset:54272
	ds_read_b128 v[242:245], v216 offset:55296
	ds_read_b128 v[246:249], v216 offset:56320
	global_load_lds_dwordx4 v[172:173], off
	v_lshl_add_u64 v[172:173], v[174:175], 0, s[28:29]
	s_add_u32 s28, s26, 0x20180
	s_mov_b32 m0, s45
	s_addc_u32 s29, s27, 0
	global_load_lds_dwordx4 v[172:173], off
	v_lshl_add_u64 v[172:173], s[28:29], 0, v[164:165]
	s_mov_b32 m0, s48
	s_nop 0
	global_load_lds_dwordx4 v[172:173], off
	v_lshl_add_u64 v[172:173], s[28:29], 0, v[166:167]
	s_mov_b32 m0, s49
	s_nop 0
	global_load_lds_dwordx4 v[172:173], off
	ds_read_b32 v162, v217
	s_mov_b32 m0, s46
	s_waitcnt lgkmcnt(0)
	v_lshl_add_u32 v162, v162, 10, v176
	global_load_lds_dwordx4 v162, s[16:17]
	ds_read_b32 v162, v217 offset:256
	s_mov_b32 m0, s47
	s_waitcnt lgkmcnt(0)
	v_lshl_add_u32 v162, v162, 10, v176
	global_load_lds_dwordx4 v162, s[16:17]
	s_waitcnt vmcnt(8) lgkmcnt(0)
	s_setprio 1
	s_barrier
	v_mfma_f32_16x16x128_f8f6f4 v[90:93], v[18:25], v[218:225], v[90:93]
	v_mfma_f32_16x16x128_f8f6f4 v[82:85], v[26:33], v[218:225], v[82:85]
	v_mfma_f32_16x16x128_f8f6f4 v[74:77], v[18:25], v[226:233], v[74:77]
	v_mfma_f32_16x16x128_f8f6f4 v[66:69], v[26:33], v[226:233], v[66:69]
	v_mfma_f32_16x16x128_f8f6f4 v[58:61], v[18:25], v[234:241], v[58:61]
	v_mfma_f32_16x16x128_f8f6f4 v[50:53], v[26:33], v[234:241], v[50:53]
	v_mfma_f32_16x16x128_f8f6f4 v[42:45], v[18:25], v[242:249], v[42:45]
	v_mfma_f32_16x16x128_f8f6f4 v[34:37], v[26:33], v[242:249], v[34:37]
	s_setprio 0
	s_setprio 1
	v_mfma_f32_16x16x128_f8f6f4 v[94:97], v[2:9], v[218:225], v[94:97]
	v_mfma_f32_16x16x128_f8f6f4 v[86:89], v[10:17], v[218:225], v[86:89]
	v_mfma_f32_16x16x128_f8f6f4 v[78:81], v[2:9], v[226:233], v[78:81]
	v_mfma_f32_16x16x128_f8f6f4 v[70:73], v[10:17], v[226:233], v[70:73]
	v_mfma_f32_16x16x128_f8f6f4 v[62:65], v[2:9], v[234:241], v[62:65]
	v_mfma_f32_16x16x128_f8f6f4 v[54:57], v[10:17], v[234:241], v[54:57]
	v_mfma_f32_16x16x128_f8f6f4 v[46:49], v[2:9], v[242:249], v[46:49]
	v_mfma_f32_16x16x128_f8f6f4 v[38:41], v[10:17], v[242:249], v[38:41]
	s_barrier
	s_setprio 0
	s_add_u32 s58, s26, 0x200
	s_addc_u32 s59, s27, 0
	s_mov_b32 s60, 0
	s_mov_b64 s[26:27], 0
.LBB0_1304:
	ds_read_b128 v[2:5], v200
	ds_read_b128 v[6:9], v201
	ds_read_b128 v[10:13], v202
	ds_read_b128 v[14:17], v203
	ds_read_b128 v[18:21], v204
	ds_read_b128 v[22:25], v205
	ds_read_b128 v[26:29], v206
	ds_read_b128 v[30:33], v207
	s_add_u32 s61, s58, s26
	s_addc_u32 s62, s59, s27
	s_add_i32 s63, s26, 0x200
	s_cmp_eq_u32 s60, 4
	s_cselect_b64 s[30:31], -1, 0
	s_and_b64 s[28:29], s[30:31], exec
	s_cselect_b32 s29, s23, s62
	s_cselect_b32 s28, s22, s61
	s_cselect_b32 s61, 0, s63
	s_and_b64 s[30:31], s[24:25], s[30:31]
	ds_read_b128 v[218:221], v216
	ds_read_b128 v[222:225], v216 offset:1024
	ds_read_b128 v[226:229], v216 offset:2048
	ds_read_b128 v[230:233], v216 offset:3072
	ds_read_b32 v162, v217 offset:512
	ds_read_b128 v[234:237], v216 offset:4096
	ds_read_b128 v[238:241], v216 offset:5120
	ds_read_b128 v[242:245], v216 offset:6144
	ds_read_b128 v[246:249], v216 offset:7168
	s_add_u32 s62, s16, s26
	s_waitcnt lgkmcnt(0)
	v_lshl_add_u32 v162, v162, 10, v176
	s_addc_u32 s63, s17, s27
	s_mov_b32 m0, s21
	s_nop 0
	global_load_lds_dwordx4 v162, s[62:63]
	ds_read_b32 v162, v217 offset:768
	s_mov_b32 m0, s57
	s_waitcnt lgkmcnt(0)
	v_lshl_add_u32 v162, v162, 10, v176
	global_load_lds_dwordx4 v162, s[62:63]
	s_waitcnt vmcnt(8) lgkmcnt(0)
	s_setprio 1
	s_barrier
	v_mfma_f32_16x16x128_f8f6f4 v[154:157], v[2:9], v[218:225], v[154:157]
	v_mfma_f32_16x16x128_f8f6f4 v[146:149], v[10:17], v[218:225], v[146:149]
	v_mfma_f32_16x16x128_f8f6f4 v[138:141], v[2:9], v[226:233], v[138:141]
	v_mfma_f32_16x16x128_f8f6f4 v[130:133], v[10:17], v[226:233], v[130:133]
	v_mfma_f32_16x16x128_f8f6f4 v[122:125], v[2:9], v[234:241], v[122:125]
	v_mfma_f32_16x16x128_f8f6f4 v[114:117], v[10:17], v[234:241], v[114:117]
	v_mfma_f32_16x16x128_f8f6f4 v[106:109], v[2:9], v[242:249], v[106:109]
	v_mfma_f32_16x16x128_f8f6f4 v[98:101], v[10:17], v[242:249], v[98:101]
	s_setprio 0
	s_setprio 1
	v_mfma_f32_16x16x128_f8f6f4 v[158:161], v[18:25], v[218:225], v[158:161]
	v_mfma_f32_16x16x128_f8f6f4 v[150:153], v[26:33], v[218:225], v[150:153]
	v_mfma_f32_16x16x128_f8f6f4 v[142:145], v[18:25], v[226:233], v[142:145]
	v_mfma_f32_16x16x128_f8f6f4 v[134:137], v[26:33], v[226:233], v[134:137]
	v_mfma_f32_16x16x128_f8f6f4 v[126:129], v[18:25], v[234:241], v[126:129]
	v_mfma_f32_16x16x128_f8f6f4 v[118:121], v[26:33], v[234:241], v[118:121]
	v_mfma_f32_16x16x128_f8f6f4 v[110:113], v[18:25], v[242:249], v[110:113]
	v_mfma_f32_16x16x128_f8f6f4 v[102:105], v[26:33], v[242:249], v[102:105]
	s_barrier
	s_setprio 0
	s_mov_b32 m0, s37
	v_lshl_add_u64 v[172:173], s[28:29], 0, v[164:165]
	s_add_u32 s62, s28, 0x20000
	ds_read_b128 v[218:221], v216 offset:16384
	ds_read_b128 v[222:225], v216 offset:17408
	ds_read_b128 v[226:229], v216 offset:18432
	ds_read_b128 v[230:233], v216 offset:19456
	ds_read_b128 v[234:237], v216 offset:20480
	ds_read_b128 v[238:241], v216 offset:21504
	ds_read_b128 v[242:245], v216 offset:22528
	ds_read_b128 v[246:249], v216 offset:23552
	global_load_lds_dwordx4 v[172:173], off
	v_lshl_add_u64 v[174:175], s[28:29], 0, v[166:167]
	s_mov_b32 m0, s38
	s_addc_u32 s63, s29, 0
	global_load_lds_dwordx4 v[174:175], off
	v_lshl_add_u64 v[250:251], s[62:63], 0, v[164:165]
	s_mov_b32 m0, s39
	s_and_b64 s[30:31], s[30:31], exec
	global_load_lds_dwordx4 v[250:251], off
	v_lshl_add_u64 v[250:251], s[62:63], 0, v[166:167]
	s_mov_b32 m0, s40
	s_cselect_b32 s30, s53, s56
	global_load_lds_dwordx4 v[250:251], off
	v_lshl_add_u32 v250, s30, 10, v177
	ds_read_b32 v162, v250
	s_add_u32 s30, s6, s61
	s_addc_u32 s31, s7, 0
	s_mov_b32 m0, s36
	s_waitcnt lgkmcnt(0)
	v_lshl_add_u32 v162, v162, 10, v176
	global_load_lds_dwordx4 v162, s[30:31]
	ds_read_b32 v162, v250 offset:256
	s_mov_b32 m0, s41
	s_waitcnt lgkmcnt(0)
	v_lshl_add_u32 v162, v162, 10, v176
	global_load_lds_dwordx4 v162, s[30:31]
	s_waitcnt vmcnt(8) lgkmcnt(0)
	s_setprio 1
	s_barrier
	v_mfma_f32_16x16x128_f8f6f4 v[90:93], v[2:9], v[218:225], v[90:93]
	v_mfma_f32_16x16x128_f8f6f4 v[82:85], v[10:17], v[218:225], v[82:85]
	v_mfma_f32_16x16x128_f8f6f4 v[74:77], v[2:9], v[226:233], v[74:77]
	v_mfma_f32_16x16x128_f8f6f4 v[66:69], v[10:17], v[226:233], v[66:69]
	v_mfma_f32_16x16x128_f8f6f4 v[58:61], v[2:9], v[234:241], v[58:61]
	v_mfma_f32_16x16x128_f8f6f4 v[50:53], v[10:17], v[234:241], v[50:53]
	v_mfma_f32_16x16x128_f8f6f4 v[42:45], v[2:9], v[242:249], v[42:45]
	v_mfma_f32_16x16x128_f8f6f4 v[34:37], v[10:17], v[242:249], v[34:37]
	s_setprio 0
	s_setprio 1
	v_mfma_f32_16x16x128_f8f6f4 v[94:97], v[18:25], v[218:225], v[94:97]
	v_mfma_f32_16x16x128_f8f6f4 v[86:89], v[26:33], v[218:225], v[86:89]
	v_mfma_f32_16x16x128_f8f6f4 v[78:81], v[18:25], v[226:233], v[78:81]
	v_mfma_f32_16x16x128_f8f6f4 v[70:73], v[26:33], v[226:233], v[70:73]
	v_mfma_f32_16x16x128_f8f6f4 v[62:65], v[18:25], v[234:241], v[62:65]
	v_mfma_f32_16x16x128_f8f6f4 v[54:57], v[26:33], v[234:241], v[54:57]
	v_mfma_f32_16x16x128_f8f6f4 v[46:49], v[18:25], v[242:249], v[46:49]
	v_mfma_f32_16x16x128_f8f6f4 v[38:41], v[26:33], v[242:249], v[38:41]
	s_barrier
	s_setprio 0
	ds_read_b128 v[10:13], v208
	ds_read_b128 v[14:17], v209
	ds_read_b128 v[26:29], v210
	ds_read_b128 v[30:33], v211
	ds_read_b128 v[2:5], v212
	ds_read_b128 v[6:9], v213
	ds_read_b128 v[18:21], v214
	ds_read_b128 v[22:25], v215
	ds_read_b128 v[218:221], v216 offset:32768
	ds_read_b128 v[222:225], v216 offset:33792
	ds_read_b128 v[226:229], v216 offset:34816
	ds_read_b128 v[230:233], v216 offset:35840
	ds_read_b32 v162, v250 offset:512
	ds_read_b128 v[234:237], v216 offset:36864
	ds_read_b128 v[238:241], v216 offset:37888
	ds_read_b128 v[242:245], v216 offset:38912
	ds_read_b128 v[246:249], v216 offset:39936
	s_waitcnt lgkmcnt(0)
	v_lshl_add_u32 v162, v162, 10, v176
	s_mov_b32 m0, s42
	s_nop 0
	global_load_lds_dwordx4 v162, s[30:31]
	ds_read_b32 v162, v250 offset:768
	s_mov_b32 m0, s43
	s_waitcnt lgkmcnt(0)
	v_lshl_add_u32 v162, v162, 10, v176
	global_load_lds_dwordx4 v162, s[30:31]
	s_waitcnt vmcnt(8) lgkmcnt(0)
	s_setprio 1
	s_barrier
	v_mfma_f32_16x16x128_f8f6f4 v[154:157], v[10:17], v[218:225], v[154:157]
	v_mfma_f32_16x16x128_f8f6f4 v[146:149], v[26:33], v[218:225], v[146:149]
	v_mfma_f32_16x16x128_f8f6f4 v[138:141], v[10:17], v[226:233], v[138:141]
	v_mfma_f32_16x16x128_f8f6f4 v[130:133], v[26:33], v[226:233], v[130:133]
	v_mfma_f32_16x16x128_f8f6f4 v[122:125], v[10:17], v[234:241], v[122:125]
	v_mfma_f32_16x16x128_f8f6f4 v[114:117], v[26:33], v[234:241], v[114:117]
	v_mfma_f32_16x16x128_f8f6f4 v[106:109], v[10:17], v[242:249], v[106:109]
	v_mfma_f32_16x16x128_f8f6f4 v[98:101], v[26:33], v[242:249], v[98:101]
	s_setprio 0
	s_setprio 1
	v_mfma_f32_16x16x128_f8f6f4 v[158:161], v[2:9], v[218:225], v[158:161]
	v_mfma_f32_16x16x128_f8f6f4 v[150:153], v[18:25], v[218:225], v[150:153]
	v_mfma_f32_16x16x128_f8f6f4 v[142:145], v[2:9], v[226:233], v[142:145]
	v_mfma_f32_16x16x128_f8f6f4 v[134:137], v[18:25], v[226:233], v[134:137]
	v_mfma_f32_16x16x128_f8f6f4 v[126:129], v[2:9], v[234:241], v[126:129]
	v_mfma_f32_16x16x128_f8f6f4 v[118:121], v[18:25], v[234:241], v[118:121]
	v_mfma_f32_16x16x128_f8f6f4 v[110:113], v[2:9], v[242:249], v[110:113]
	v_mfma_f32_16x16x128_f8f6f4 v[102:105], v[18:25], v[242:249], v[102:105]
	s_barrier
	s_setprio 0
	s_mov_b32 m0, s44
	v_lshl_add_u64 v[172:173], v[172:173], 0, s[90:91]
	s_add_u32 s28, s28, 0x20080
	ds_read_b128 v[218:221], v216 offset:49152
	ds_read_b128 v[222:225], v216 offset:50176
	ds_read_b128 v[226:229], v216 offset:51200
	ds_read_b128 v[230:233], v216 offset:52224
	ds_read_b128 v[234:237], v216 offset:53248
	ds_read_b128 v[238:241], v216 offset:54272
	ds_read_b128 v[242:245], v216 offset:55296
	ds_read_b128 v[246:249], v216 offset:56320
	global_load_lds_dwordx4 v[172:173], off
	v_lshl_add_u64 v[172:173], v[174:175], 0, s[90:91]
	s_mov_b32 m0, s45
	s_addc_u32 s29, s29, 0
	global_load_lds_dwordx4 v[172:173], off
	v_lshl_add_u64 v[172:173], s[28:29], 0, v[164:165]
	s_mov_b32 m0, s48
	s_nop 0
	global_load_lds_dwordx4 v[172:173], off
	v_lshl_add_u64 v[172:173], s[28:29], 0, v[166:167]
	s_mov_b32 m0, s49
	s_nop 0
	global_load_lds_dwordx4 v[172:173], off
	ds_read_b32 v162, v250
	s_mov_b32 m0, s46
	s_waitcnt lgkmcnt(0)
	v_lshl_add_u32 v162, v162, 10, v176
	v_lshl_add_u64 v[172:173], s[30:31], 0, v[162:163]
	v_lshl_add_u64 v[172:173], v[172:173], 0, s[90:91]
	global_load_lds_dwordx4 v[172:173], off
	ds_read_b32 v162, v250 offset:256
	s_mov_b32 m0, s47
	s_waitcnt lgkmcnt(0)
	v_lshl_add_u32 v162, v162, 10, v176
	v_lshl_add_u64 v[172:173], s[30:31], 0, v[162:163]
	v_lshl_add_u64 v[172:173], v[172:173], 0, s[90:91]
	global_load_lds_dwordx4 v[172:173], off
	s_waitcnt vmcnt(8) lgkmcnt(0)
	s_setprio 1
	s_barrier
	v_mfma_f32_16x16x128_f8f6f4 v[90:93], v[10:17], v[218:225], v[90:93]
	v_mfma_f32_16x16x128_f8f6f4 v[82:85], v[26:33], v[218:225], v[82:85]
	v_mfma_f32_16x16x128_f8f6f4 v[74:77], v[10:17], v[226:233], v[74:77]
	v_mfma_f32_16x16x128_f8f6f4 v[66:69], v[26:33], v[226:233], v[66:69]
	v_mfma_f32_16x16x128_f8f6f4 v[58:61], v[10:17], v[234:241], v[58:61]
	v_mfma_f32_16x16x128_f8f6f4 v[50:53], v[26:33], v[234:241], v[50:53]
	v_mfma_f32_16x16x128_f8f6f4 v[42:45], v[10:17], v[242:249], v[42:45]
	v_mfma_f32_16x16x128_f8f6f4 v[34:37], v[26:33], v[242:249], v[34:37]
	s_setprio 0
	s_setprio 1
	v_mfma_f32_16x16x128_f8f6f4 v[94:97], v[2:9], v[218:225], v[94:97]
	v_mfma_f32_16x16x128_f8f6f4 v[86:89], v[18:25], v[218:225], v[86:89]
	v_mfma_f32_16x16x128_f8f6f4 v[78:81], v[2:9], v[226:233], v[78:81]
	v_mfma_f32_16x16x128_f8f6f4 v[70:73], v[18:25], v[226:233], v[70:73]
	v_mfma_f32_16x16x128_f8f6f4 v[62:65], v[2:9], v[234:241], v[62:65]
	v_mfma_f32_16x16x128_f8f6f4 v[54:57], v[18:25], v[234:241], v[54:57]
	v_mfma_f32_16x16x128_f8f6f4 v[46:49], v[2:9], v[242:249], v[46:49]
	v_mfma_f32_16x16x128_f8f6f4 v[38:41], v[18:25], v[242:249], v[38:41]
	s_barrier
	s_setprio 0
	s_add_i32 s60, s60, 2
	s_add_u32 s26, s26, 0x100
	s_addc_u32 s27, s27, 0
	s_cmp_lt_u32 s60, 6
	s_cbranch_scc1 .LBB0_1304
	s_andn2_b64 vcc, exec, s[18:19]
	s_cbranch_vccnz .LBB0_1307
	s_barrier

.LBB0_1373:
	ds_read_b128 v[2:5], v202
	ds_read_b128 v[6:9], v203
	ds_read_b128 v[10:13], v204
	ds_read_b128 v[14:17], v205
	ds_read_b128 v[18:21], v206
	ds_read_b128 v[22:25], v207
	ds_read_b128 v[26:29], v208
	ds_read_b128 v[30:33], v209
	s_ashr_i32 s13, s12, 31
	s_lshl_b64 s[16:17], s[12:13], 19
	s_add_u32 s16, s27, s16
	s_addc_u32 s17, s28, s17
	s_and_b64 s[24:25], s[24:25], exec
	s_cselect_b32 s11, s17, s23
	s_cselect_b32 s13, s16, s22
	s_add_u32 s24, s22, 0x40080
	s_addc_u32 s25, s23, 0
	s_add_i32 s47, s31, 0xc000
	v_lshl_add_u64 v[66:67], s[24:25], 0, v[162:163]
	s_mov_b32 m0, s47
	s_add_i32 s48, s31, 0xe000
	ds_read_b128 v[34:37], v218
	ds_read_b128 v[38:41], v218 offset:1024
	ds_read_b128 v[42:45], v218 offset:2048
	ds_read_b128 v[46:49], v218 offset:3072
	ds_read_b128 v[50:53], v218 offset:4096
	ds_read_b128 v[54:57], v218 offset:5120
	ds_read_b128 v[58:61], v218 offset:6144
	ds_read_b128 v[62:65], v218 offset:7168
	global_load_lds_dwordx4 v[66:67], off
	v_lshl_add_u64 v[66:67], s[24:25], 0, v[164:165]
	s_mov_b32 m0, s48
	s_nop 0
	global_load_lds_dwordx4 v[66:67], off
	s_waitcnt vmcnt(8) lgkmcnt(0)
	s_setprio 1
	s_barrier
	v_mfma_f32_16x16x128_f8f6f4 v[158:161], v[2:9], v[34:41], 0
	v_mfma_f32_16x16x128_f8f6f4 v[154:157], v[10:17], v[34:41], 0
	v_mfma_f32_16x16x128_f8f6f4 v[150:153], v[2:9], v[42:49], 0
	v_mfma_f32_16x16x128_f8f6f4 v[146:149], v[10:17], v[42:49], 0
	v_mfma_f32_16x16x128_f8f6f4 v[126:129], v[2:9], v[50:57], 0
	v_mfma_f32_16x16x128_f8f6f4 v[122:125], v[10:17], v[50:57], 0
	v_mfma_f32_16x16x128_f8f6f4 v[118:121], v[2:9], v[58:65], 0
	v_mfma_f32_16x16x128_f8f6f4 v[114:117], v[10:17], v[58:65], 0
	s_setprio 0
	s_setprio 1
	v_mfma_f32_16x16x128_f8f6f4 v[142:145], v[18:25], v[34:41], 0
	v_mfma_f32_16x16x128_f8f6f4 v[138:141], v[26:33], v[34:41], 0
	v_mfma_f32_16x16x128_f8f6f4 v[134:137], v[18:25], v[42:49], 0
	v_mfma_f32_16x16x128_f8f6f4 v[130:133], v[26:33], v[42:49], 0
	v_mfma_f32_16x16x128_f8f6f4 v[110:113], v[18:25], v[50:57], 0
	v_mfma_f32_16x16x128_f8f6f4 v[106:109], v[26:33], v[50:57], 0
	v_mfma_f32_16x16x128_f8f6f4 v[98:101], v[18:25], v[58:65], 0
	v_mfma_f32_16x16x128_f8f6f4 v[90:93], v[26:33], v[58:65], 0
	s_barrier
	s_setprio 0
	v_lshl_add_u64 v[172:173], s[20:21], 0, v[162:163]
	s_mov_b64 s[50:51], 0x100
	s_mov_b32 m0, s33
	v_lshl_add_u64 v[50:51], v[172:173], 0, s[50:51]
	v_lshl_add_u64 v[174:175], s[20:21], 0, v[164:165]
	s_add_u32 s24, s20, 0x40100
	ds_read_b128 v[34:37], v218 offset:16384
	ds_read_b128 v[38:41], v218 offset:17408
	ds_read_b128 v[42:45], v218 offset:18432
	ds_read_b128 v[46:49], v218 offset:19456
	ds_read_b128 v[220:223], v218 offset:20480
	ds_read_b128 v[224:227], v218 offset:21504
	ds_read_b128 v[228:231], v218 offset:22528
	ds_read_b128 v[232:235], v218 offset:23552
	global_load_lds_dwordx4 v[50:51], off
	v_lshl_add_u64 v[50:51], v[174:175], 0, s[50:51]
	s_mov_b32 m0, s34
	s_addc_u32 s25, s21, 0
	global_load_lds_dwordx4 v[50:51], off
	v_lshl_add_u64 v[50:51], s[24:25], 0, v[162:163]
	s_mov_b32 m0, s35
	v_lshl_add_u64 v[176:177], s[22:23], 0, v[162:163]
	global_load_lds_dwordx4 v[50:51], off
	v_lshl_add_u64 v[50:51], s[24:25], 0, v[164:165]
	s_mov_b32 m0, s36
	v_lshl_add_u64 v[178:179], s[22:23], 0, v[164:165]
	global_load_lds_dwordx4 v[50:51], off
	v_lshl_add_u64 v[50:51], v[176:177], 0, s[50:51]
	s_mov_b32 m0, s31
	s_nop 0
	global_load_lds_dwordx4 v[50:51], off
	v_lshl_add_u64 v[50:51], v[178:179], 0, s[50:51]
	s_mov_b32 m0, s37
	s_nop 0
	global_load_lds_dwordx4 v[50:51], off
	s_waitcnt vmcnt(8) lgkmcnt(0)
	s_setprio 1
	s_barrier
	v_mfma_f32_16x16x128_f8f6f4 v[102:105], v[2:9], v[34:41], 0
	v_mfma_f32_16x16x128_f8f6f4 v[94:97], v[10:17], v[34:41], 0
	v_mfma_f32_16x16x128_f8f6f4 v[86:89], v[2:9], v[42:49], 0
	v_mfma_f32_16x16x128_f8f6f4 v[82:85], v[10:17], v[42:49], 0
	v_mfma_f32_16x16x128_f8f6f4 v[62:65], v[2:9], v[220:227], 0
	v_mfma_f32_16x16x128_f8f6f4 v[58:61], v[10:17], v[220:227], 0
	v_mfma_f32_16x16x128_f8f6f4 v[54:57], v[2:9], v[228:235], 0
	v_mfma_f32_16x16x128_f8f6f4 v[50:53], v[10:17], v[228:235], 0
	s_setprio 0
	s_setprio 1
	v_mfma_f32_16x16x128_f8f6f4 v[78:81], v[18:25], v[34:41], 0
	v_mfma_f32_16x16x128_f8f6f4 v[74:77], v[26:33], v[34:41], 0
	v_mfma_f32_16x16x128_f8f6f4 v[70:73], v[18:25], v[42:49], 0
	v_mfma_f32_16x16x128_f8f6f4 v[66:69], v[26:33], v[42:49], 0
	v_mfma_f32_16x16x128_f8f6f4 v[46:49], v[18:25], v[220:227], 0
	v_mfma_f32_16x16x128_f8f6f4 v[42:45], v[26:33], v[220:227], 0
	v_mfma_f32_16x16x128_f8f6f4 v[38:41], v[18:25], v[228:235], 0
	v_mfma_f32_16x16x128_f8f6f4 v[34:37], v[26:33], v[228:235], 0
	s_barrier
	s_setprio 0
	ds_read_b128 v[18:21], v210
	ds_read_b128 v[22:25], v211
	ds_read_b128 v[26:29], v212
	ds_read_b128 v[30:33], v213
	ds_read_b128 v[2:5], v214
	ds_read_b128 v[6:9], v215
	ds_read_b128 v[10:13], v216
	ds_read_b128 v[14:17], v217
	s_add_u32 s24, s22, 0x40100
	s_addc_u32 s25, s23, 0
	s_mov_b32 m0, s38
	v_lshl_add_u64 v[252:253], s[24:25], 0, v[162:163]
	ds_read_b128 v[220:223], v218 offset:32768
	ds_read_b128 v[224:227], v218 offset:33792
	ds_read_b128 v[228:231], v218 offset:34816
	ds_read_b128 v[232:235], v218 offset:35840
	ds_read_b128 v[236:239], v218 offset:36864
	ds_read_b128 v[240:243], v218 offset:37888
	ds_read_b128 v[244:247], v218 offset:38912
	ds_read_b128 v[248:251], v218 offset:39936
	global_load_lds_dwordx4 v[252:253], off
	v_lshl_add_u64 v[252:253], s[24:25], 0, v[164:165]
	s_mov_b32 m0, s39
	s_nop 0
	global_load_lds_dwordx4 v[252:253], off
	s_waitcnt vmcnt(8) lgkmcnt(0)
	s_setprio 1
	s_barrier
	v_mfma_f32_16x16x128_f8f6f4 v[158:161], v[18:25], v[220:227], v[158:161]
	v_mfma_f32_16x16x128_f8f6f4 v[154:157], v[26:33], v[220:227], v[154:157]
	v_mfma_f32_16x16x128_f8f6f4 v[150:153], v[18:25], v[228:235], v[150:153]
	v_mfma_f32_16x16x128_f8f6f4 v[146:149], v[26:33], v[228:235], v[146:149]
	v_mfma_f32_16x16x128_f8f6f4 v[126:129], v[18:25], v[236:243], v[126:129]
	v_mfma_f32_16x16x128_f8f6f4 v[122:125], v[26:33], v[236:243], v[122:125]
	v_mfma_f32_16x16x128_f8f6f4 v[118:121], v[18:25], v[244:251], v[118:121]
	v_mfma_f32_16x16x128_f8f6f4 v[114:117], v[26:33], v[244:251], v[114:117]
	s_setprio 0
	s_setprio 1
	v_mfma_f32_16x16x128_f8f6f4 v[142:145], v[2:9], v[220:227], v[142:145]
	v_mfma_f32_16x16x128_f8f6f4 v[138:141], v[10:17], v[220:227], v[138:141]
	v_mfma_f32_16x16x128_f8f6f4 v[134:137], v[2:9], v[228:235], v[134:137]
	v_mfma_f32_16x16x128_f8f6f4 v[130:133], v[10:17], v[228:235], v[130:133]
	v_mfma_f32_16x16x128_f8f6f4 v[110:113], v[2:9], v[236:243], v[110:113]
	v_mfma_f32_16x16x128_f8f6f4 v[106:109], v[10:17], v[236:243], v[106:109]
	v_mfma_f32_16x16x128_f8f6f4 v[98:101], v[2:9], v[244:251], v[98:101]
	v_mfma_f32_16x16x128_f8f6f4 v[90:93], v[10:17], v[244:251], v[90:93]
	s_barrier
	s_setprio 0
	s_mov_b64 s[50:51], 0x180
	s_mov_b32 m0, s40
	v_lshl_add_u64 v[172:173], v[172:173], 0, s[50:51]
	s_add_u32 s24, s20, 0x40180
	ds_read_b128 v[220:223], v218 offset:49152
	ds_read_b128 v[224:227], v218 offset:50176
	ds_read_b128 v[228:231], v218 offset:51200
	ds_read_b128 v[232:235], v218 offset:52224
	ds_read_b128 v[236:239], v218 offset:53248
	ds_read_b128 v[240:243], v218 offset:54272
	ds_read_b128 v[244:247], v218 offset:55296
	ds_read_b128 v[248:251], v218 offset:56320
	global_load_lds_dwordx4 v[172:173], off
	v_lshl_add_u64 v[172:173], v[174:175], 0, s[50:51]
	s_mov_b32 m0, s41
	s_addc_u32 s25, s21, 0
	global_load_lds_dwordx4 v[172:173], off
	v_lshl_add_u64 v[172:173], s[24:25], 0, v[162:163]
	s_mov_b32 m0, s44
	s_nop 0
	global_load_lds_dwordx4 v[172:173], off
	v_lshl_add_u64 v[172:173], s[24:25], 0, v[164:165]
	s_mov_b32 m0, s45
	s_nop 0
	global_load_lds_dwordx4 v[172:173], off
	v_lshl_add_u64 v[172:173], v[176:177], 0, s[50:51]
	s_mov_b32 m0, s42
	s_nop 0
	global_load_lds_dwordx4 v[172:173], off
	v_lshl_add_u64 v[172:173], v[178:179], 0, s[50:51]
	s_mov_b32 m0, s43
	s_nop 0
	global_load_lds_dwordx4 v[172:173], off
	s_waitcnt vmcnt(8) lgkmcnt(0)
	s_setprio 1
	s_barrier
	v_mfma_f32_16x16x128_f8f6f4 v[102:105], v[18:25], v[220:227], v[102:105]
	v_mfma_f32_16x16x128_f8f6f4 v[94:97], v[26:33], v[220:227], v[94:97]
	v_mfma_f32_16x16x128_f8f6f4 v[86:89], v[18:25], v[228:235], v[86:89]
	v_mfma_f32_16x16x128_f8f6f4 v[82:85], v[26:33], v[228:235], v[82:85]
	v_mfma_f32_16x16x128_f8f6f4 v[62:65], v[18:25], v[236:243], v[62:65]
	v_mfma_f32_16x16x128_f8f6f4 v[58:61], v[26:33], v[236:243], v[58:61]
	v_mfma_f32_16x16x128_f8f6f4 v[54:57], v[18:25], v[244:251], v[54:57]
	v_mfma_f32_16x16x128_f8f6f4 v[50:53], v[26:33], v[244:251], v[50:53]
	s_setprio 0
	s_setprio 1
	v_mfma_f32_16x16x128_f8f6f4 v[78:81], v[2:9], v[220:227], v[78:81]
	v_mfma_f32_16x16x128_f8f6f4 v[74:77], v[10:17], v[220:227], v[74:77]
	v_mfma_f32_16x16x128_f8f6f4 v[70:73], v[2:9], v[228:235], v[70:73]
	v_mfma_f32_16x16x128_f8f6f4 v[66:69], v[10:17], v[228:235], v[66:69]
	v_mfma_f32_16x16x128_f8f6f4 v[46:49], v[2:9], v[236:243], v[46:49]
	v_mfma_f32_16x16x128_f8f6f4 v[42:45], v[10:17], v[236:243], v[42:45]
	v_mfma_f32_16x16x128_f8f6f4 v[38:41], v[2:9], v[244:251], v[38:41]
	v_mfma_f32_16x16x128_f8f6f4 v[34:37], v[10:17], v[244:251], v[34:37]
	s_barrier
	s_setprio 0
	s_add_u32 s49, s20, 0x200
	s_addc_u32 s50, s21, 0
	s_add_u32 s20, s22, 0x40180
	s_addc_u32 s21, s23, 0
	s_mov_b32 s51, 0
.LBB0_1374:
	ds_read_b128 v[2:5], v202
	ds_read_b128 v[6:9], v203
	ds_read_b128 v[18:21], v204
	ds_read_b128 v[22:25], v205
	ds_read_b128 v[26:29], v206
	ds_read_b128 v[30:33], v207
	ds_read_b128 v[172:175], v208
	ds_read_b128 v[176:179], v209
	ds_read_b128 v[10:13], v218
	ds_read_b128 v[14:17], v218 offset:1024
	ds_read_b128 v[220:223], v218 offset:2048
	ds_read_b128 v[224:227], v218 offset:3072
	ds_read_b128 v[228:231], v218 offset:4096
	ds_read_b128 v[232:235], v218 offset:5120
	ds_read_b128 v[236:239], v218 offset:6144
	ds_read_b128 v[240:243], v218 offset:7168
	s_add_u32 s22, s20, 0xfffc0080
	s_addc_u32 s23, s21, -1
	s_cmp_eq_u32 s51, 12
	s_cselect_b32 s25, s11, s23
	s_cselect_b32 s24, s13, s22
	s_cselect_b32 s23, s15, s50
	s_cselect_b32 s22, s14, s49
	s_mov_b32 m0, s47
	v_lshl_add_u64 v[244:245], s[20:21], 0, v[170:171]
	global_load_lds_dwordx4 v[244:245], off
	v_lshl_add_u64 v[244:245], s[20:21], 0, v[168:169]
	s_mov_b32 m0, s48
	s_nop 0
	global_load_lds_dwordx4 v[244:245], off
	s_waitcnt vmcnt(8) lgkmcnt(0)
	s_setprio 1
	s_barrier
	v_mfma_f32_16x16x128_f8f6f4 v[158:161], v[2:9], v[10:17], v[158:161]
	v_mfma_f32_16x16x128_f8f6f4 v[154:157], v[18:25], v[10:17], v[154:157]
	v_mfma_f32_16x16x128_f8f6f4 v[150:153], v[2:9], v[220:227], v[150:153]
	v_mfma_f32_16x16x128_f8f6f4 v[146:149], v[18:25], v[220:227], v[146:149]
	v_mfma_f32_16x16x128_f8f6f4 v[126:129], v[2:9], v[228:235], v[126:129]
	v_mfma_f32_16x16x128_f8f6f4 v[122:125], v[18:25], v[228:235], v[122:125]
	v_mfma_f32_16x16x128_f8f6f4 v[118:121], v[2:9], v[236:243], v[118:121]
	v_mfma_f32_16x16x128_f8f6f4 v[114:117], v[18:25], v[236:243], v[114:117]
	s_setprio 0
	s_setprio 1
	v_mfma_f32_16x16x128_f8f6f4 v[142:145], v[26:33], v[10:17], v[142:145]
	v_mfma_f32_16x16x128_f8f6f4 v[138:141], v[172:179], v[10:17], v[138:141]
	v_mfma_f32_16x16x128_f8f6f4 v[134:137], v[26:33], v[220:227], v[134:137]
	v_mfma_f32_16x16x128_f8f6f4 v[130:133], v[172:179], v[220:227], v[130:133]
	v_mfma_f32_16x16x128_f8f6f4 v[110:113], v[26:33], v[228:235], v[110:113]
	v_mfma_f32_16x16x128_f8f6f4 v[106:109], v[172:179], v[228:235], v[106:109]
	v_mfma_f32_16x16x128_f8f6f4 v[98:101], v[26:33], v[236:243], v[98:101]
	v_mfma_f32_16x16x128_f8f6f4 v[90:93], v[172:179], v[236:243], v[90:93]
	s_barrier
	s_setprio 0
	ds_read_b128 v[220:223], v218 offset:16384
	ds_read_b128 v[224:227], v218 offset:17408
	ds_read_b128 v[228:231], v218 offset:18432
	ds_read_b128 v[232:235], v218 offset:19456
	ds_read_b128 v[236:239], v218 offset:20480
	ds_read_b128 v[240:243], v218 offset:21504
	ds_read_b128 v[244:247], v218 offset:22528
	ds_read_b128 v[248:251], v218 offset:23552
	s_mov_b32 m0, s33
	v_lshl_add_u64 v[10:11], s[22:23], 0, v[162:163]
	s_add_u32 s52, s22, 0x40000
	global_load_lds_dwordx4 v[10:11], off
	v_lshl_add_u64 v[12:13], s[22:23], 0, v[164:165]
	s_mov_b32 m0, s34
	s_addc_u32 s53, s23, 0
	global_load_lds_dwordx4 v[12:13], off
	v_lshl_add_u64 v[14:15], s[52:53], 0, v[162:163]
	s_mov_b32 m0, s35
	v_lshl_add_u64 v[16:17], s[24:25], 0, v[164:165]
	global_load_lds_dwordx4 v[14:15], off
	v_lshl_add_u64 v[14:15], s[52:53], 0, v[164:165]
	s_mov_b32 m0, s36
	s_nop 0
	global_load_lds_dwordx4 v[14:15], off
	v_lshl_add_u64 v[14:15], s[24:25], 0, v[162:163]
	s_mov_b32 m0, s31
	s_nop 0
	global_load_lds_dwordx4 v[14:15], off
	s_mov_b32 m0, s37
	s_nop 0
	global_load_lds_dwordx4 v[16:17], off
	s_waitcnt vmcnt(8) lgkmcnt(0)
	s_setprio 1
	s_barrier
	v_mfma_f32_16x16x128_f8f6f4 v[102:105], v[2:9], v[220:227], v[102:105]
	v_mfma_f32_16x16x128_f8f6f4 v[94:97], v[18:25], v[220:227], v[94:97]
	v_mfma_f32_16x16x128_f8f6f4 v[86:89], v[2:9], v[228:235], v[86:89]
	v_mfma_f32_16x16x128_f8f6f4 v[82:85], v[18:25], v[228:235], v[82:85]
	v_mfma_f32_16x16x128_f8f6f4 v[62:65], v[2:9], v[236:243], v[62:65]
	v_mfma_f32_16x16x128_f8f6f4 v[58:61], v[18:25], v[236:243], v[58:61]
	v_mfma_f32_16x16x128_f8f6f4 v[54:57], v[2:9], v[244:251], v[54:57]
	v_mfma_f32_16x16x128_f8f6f4 v[50:53], v[18:25], v[244:251], v[50:53]
	s_setprio 0
	s_setprio 1
	v_mfma_f32_16x16x128_f8f6f4 v[78:81], v[26:33], v[220:227], v[78:81]
	v_mfma_f32_16x16x128_f8f6f4 v[74:77], v[172:179], v[220:227], v[74:77]
	v_mfma_f32_16x16x128_f8f6f4 v[70:73], v[26:33], v[228:235], v[70:73]
	v_mfma_f32_16x16x128_f8f6f4 v[66:69], v[172:179], v[228:235], v[66:69]
	v_mfma_f32_16x16x128_f8f6f4 v[46:49], v[26:33], v[236:243], v[46:49]
	v_mfma_f32_16x16x128_f8f6f4 v[42:45], v[172:179], v[236:243], v[42:45]
	v_mfma_f32_16x16x128_f8f6f4 v[38:41], v[26:33], v[244:251], v[38:41]
	v_mfma_f32_16x16x128_f8f6f4 v[34:37], v[172:179], v[244:251], v[34:37]
	s_barrier
	s_setprio 0
	ds_read_b128 v[18:21], v210
	ds_read_b128 v[22:25], v211
	ds_read_b128 v[26:29], v212
	ds_read_b128 v[30:33], v213
	ds_read_b128 v[2:5], v214
	ds_read_b128 v[6:9], v215
	ds_read_b128 v[172:175], v216
	ds_read_b128 v[176:179], v217
	ds_read_b128 v[220:223], v218 offset:32768
	ds_read_b128 v[224:227], v218 offset:33792
	ds_read_b128 v[228:231], v218 offset:34816
	ds_read_b128 v[232:235], v218 offset:35840
	ds_read_b128 v[236:239], v218 offset:36864
	ds_read_b128 v[240:243], v218 offset:37888
	ds_read_b128 v[244:247], v218 offset:38912
	ds_read_b128 v[248:251], v218 offset:39936
	s_add_u32 s24, s24, 0x40000
	s_addc_u32 s25, s25, 0
	s_mov_b32 m0, s38
	v_lshl_add_u64 v[252:253], s[24:25], 0, v[162:163]
	global_load_lds_dwordx4 v[252:253], off
	v_lshl_add_u64 v[252:253], s[24:25], 0, v[164:165]
	s_mov_b32 m0, s39
	s_nop 0
	global_load_lds_dwordx4 v[252:253], off
	s_waitcnt vmcnt(8) lgkmcnt(0)
	s_setprio 1
	s_barrier
	v_mfma_f32_16x16x128_f8f6f4 v[158:161], v[18:25], v[220:227], v[158:161]
	v_mfma_f32_16x16x128_f8f6f4 v[154:157], v[26:33], v[220:227], v[154:157]
	v_mfma_f32_16x16x128_f8f6f4 v[150:153], v[18:25], v[228:235], v[150:153]
	v_mfma_f32_16x16x128_f8f6f4 v[146:149], v[26:33], v[228:235], v[146:149]
	v_mfma_f32_16x16x128_f8f6f4 v[126:129], v[18:25], v[236:243], v[126:129]
	v_mfma_f32_16x16x128_f8f6f4 v[122:125], v[26:33], v[236:243], v[122:125]
	v_mfma_f32_16x16x128_f8f6f4 v[118:121], v[18:25], v[244:251], v[118:121]
	v_mfma_f32_16x16x128_f8f6f4 v[114:117], v[26:33], v[244:251], v[114:117]
	s_setprio 0
	s_setprio 1
	v_mfma_f32_16x16x128_f8f6f4 v[142:145], v[2:9], v[220:227], v[142:145]
	v_mfma_f32_16x16x128_f8f6f4 v[138:141], v[172:179], v[220:227], v[138:141]
	v_mfma_f32_16x16x128_f8f6f4 v[134:137], v[2:9], v[228:235], v[134:137]
	v_mfma_f32_16x16x128_f8f6f4 v[130:133], v[172:179], v[228:235], v[130:133]
	v_mfma_f32_16x16x128_f8f6f4 v[110:113], v[2:9], v[236:243], v[110:113]
	v_mfma_f32_16x16x128_f8f6f4 v[106:109], v[172:179], v[236:243], v[106:109]
	v_mfma_f32_16x16x128_f8f6f4 v[98:101], v[2:9], v[244:251], v[98:101]
	v_mfma_f32_16x16x128_f8f6f4 v[90:93], v[172:179], v[244:251], v[90:93]
	s_barrier
	s_setprio 0
	ds_read_b128 v[220:223], v218 offset:49152
	ds_read_b128 v[224:227], v218 offset:50176
	ds_read_b128 v[228:231], v218 offset:51200
	ds_read_b128 v[232:235], v218 offset:52224
	ds_read_b128 v[236:239], v218 offset:53248
	ds_read_b128 v[240:243], v218 offset:54272
	ds_read_b128 v[244:247], v218 offset:55296
	ds_read_b128 v[248:251], v218 offset:56320
	s_mov_b32 m0, s40
	v_lshl_add_u64 v[10:11], v[10:11], 0, s[90:91]
	s_add_u32 s22, s22, 0x40080
	global_load_lds_dwordx4 v[10:11], off
	v_lshl_add_u64 v[10:11], v[12:13], 0, s[90:91]
	s_mov_b32 m0, s41
	s_addc_u32 s23, s23, 0
	global_load_lds_dwordx4 v[10:11], off
	v_lshl_add_u64 v[10:11], s[22:23], 0, v[162:163]
	s_mov_b32 m0, s44
	s_nop 0
	global_load_lds_dwordx4 v[10:11], off
	v_lshl_add_u64 v[10:11], s[22:23], 0, v[164:165]
	s_mov_b32 m0, s45
	s_nop 0
	global_load_lds_dwordx4 v[10:11], off
	v_lshl_add_u64 v[10:11], v[14:15], 0, s[90:91]
	s_mov_b32 m0, s42
	s_nop 0
	global_load_lds_dwordx4 v[10:11], off
	v_lshl_add_u64 v[10:11], v[16:17], 0, s[90:91]
	s_mov_b32 m0, s43
	s_nop 0
	global_load_lds_dwordx4 v[10:11], off
	s_waitcnt vmcnt(8) lgkmcnt(0)
	s_setprio 1
	s_barrier
	v_mfma_f32_16x16x128_f8f6f4 v[102:105], v[18:25], v[220:227], v[102:105]
	v_mfma_f32_16x16x128_f8f6f4 v[94:97], v[26:33], v[220:227], v[94:97]
	v_mfma_f32_16x16x128_f8f6f4 v[86:89], v[18:25], v[228:235], v[86:89]
	v_mfma_f32_16x16x128_f8f6f4 v[82:85], v[26:33], v[228:235], v[82:85]
	v_mfma_f32_16x16x128_f8f6f4 v[62:65], v[18:25], v[236:243], v[62:65]
	v_mfma_f32_16x16x128_f8f6f4 v[58:61], v[26:33], v[236:243], v[58:61]
	v_mfma_f32_16x16x128_f8f6f4 v[54:57], v[18:25], v[244:251], v[54:57]
	v_mfma_f32_16x16x128_f8f6f4 v[50:53], v[26:33], v[244:251], v[50:53]
	s_setprio 0
	s_setprio 1
	v_mfma_f32_16x16x128_f8f6f4 v[78:81], v[2:9], v[220:227], v[78:81]
	v_mfma_f32_16x16x128_f8f6f4 v[74:77], v[172:179], v[220:227], v[74:77]
	v_mfma_f32_16x16x128_f8f6f4 v[70:73], v[2:9], v[228:235], v[70:73]
	v_mfma_f32_16x16x128_f8f6f4 v[66:69], v[172:179], v[228:235], v[66:69]
	v_mfma_f32_16x16x128_f8f6f4 v[46:49], v[2:9], v[236:243], v[46:49]
	v_mfma_f32_16x16x128_f8f6f4 v[42:45], v[172:179], v[236:243], v[42:45]
	v_mfma_f32_16x16x128_f8f6f4 v[38:41], v[2:9], v[244:251], v[38:41]
	v_mfma_f32_16x16x128_f8f6f4 v[34:37], v[172:179], v[244:251], v[34:37]
	s_barrier
	s_setprio 0
	s_add_i32 s51, s51, 2
	s_add_u32 s49, s49, 0x100
	s_addc_u32 s50, s50, 0
	s_add_u32 s20, s20, 0x100
	s_addc_u32 s21, s21, 0
	s_cmp_lt_u32 s51, 14
	s_cbranch_scc1 .LBB0_1374
	s_andn2_b64 vcc, exec, s[8:9]
	s_cbranch_vccnz .LBB0_1377
	s_barrier
